# GEMM K-loops P2/P4/P7: first two sub-phase waits after an epilogue no longer retire the epilogue stores (vmcnt 8+nst under a flag)
# baseline (speedup 1.0000x reference)
; #define PG8_STAGE(bufoff, gbase, voff) do { _Pragma("unroll") for (int _i = 0; _i < 2; ++_i) { unsigned keep_; \
;         asm volatile("s_mov_b32 %0, m0\n\ts_mov_b32 m0, %3\n\ts_nop 0\n\tglobal_load_lds_dwordx4 %1, %2\n\ts_mov_b32 m0, %0" : "=&s"(keep_) : "v"((voff)[_i]), "s"((const char*)(gbase)), "s"(ldsb + (unsigned)((bufoff) + _i * 8192)) : "memory"); } } while (0)
; #define PG8_WAIT_V(n) asm volatile("s_waitcnt vmcnt(" #n ")" ::: "memory")
; #define PG8_BAR __builtin_amdgcn_s_barrier()
; template <class Epi, class Sched, bool ALIGN_EPI, bool FP8 = false>
; __device__ __forceinline__ void gemm_phase(PG8_LAS unsigned char* lds, const Gemm g, const Sched& S, const Epi& E, const int wid, const int lane) {
;     ...
;     const int tid = wid * 64 + lane, wr = wid >> 2, wc = wid & 3, fr = lane & 15, fq = lane >> 4;
;     int KB = g.KB; asm volatile("" : "+s"(KB)); const int nt = KB / 128;
;     unsigned voffA[2], voffB[2]; int rA[2]; unsigned cA2[2];
; #pragma unroll
;     for (int i = 0; i < 2; ++i) { int R, C; stage_rc(tid * 16 + i * 8192, R, C); const int Rb = Epi::PERM ? ((R & ~31) + perm32(R & 31)) : R;
;         rA[i] = R; cA2[i] = (unsigned)C * 2u; voffA[i] = (unsigned)(R * KB + C * 2); voffB[i] = (unsigned)(Rb * KB + C * 2); }
;     const size_t kstep = (size_t)(BK * 2);
;     const size_t hstep = (size_t)HALF * KB;
;     const size_t hstepA = GA ? (size_t)0 : hstep;
;     const size_t tstep = 2 * hstep;
;     const unsigned ldsw = (unsigned)wid * 1024u;
;     const int aoff = lds_byte(wr * 64 + fr, fq * 8), boff = lds_byte(wc * 32 + fr, fq * 8);
;     ...
;     const char* cA = GA ? (const char*)g.A : (const char*)g.A + (size_t)cur.pm * tstep; const char* cB = (const char*)g.Bt + (size_t)cur.pn * tstep;
;     PG8_STAGE(PG8_SB(0, 0), cB, voffB); PG8_STAGE(PG8_SB(0, 1), cB + hstep, voffB); PG8_STAGE(PG8_SA(0, 0), cA, vc0); PG8_STAGE(PG8_SA(0, 1), cA + hstepA, vc1);
;     if (wr == 1) PG8_BAR;
;     PG8_WAIT_V(2); PG8_BAR;
;     PG8_STAGE(PG8_SB(1, 0), cB + kstep, voffB); PG8_STAGE(PG8_SA(1, 0), cA + kstep, vc0); PG8_STAGE(PG8_SB(1, 1), cB + hstep + kstep, voffB);
;     PG8_WAIT_V(6); PG8_BAR;
.LBB0_213:
	s_lshr_b32 s1, s1, 25
	s_bfe_u32 s13, s90, 0x20006
	s_add_i32 s1, s0, s1
	s_ashr_i32 s46, s1, 7
	s_lshl_b32 s47, s12, 6
	v_and_b32_e32 v0, 0xfffffc00, v0
	s_lshl_b32 s1, s13, 5
	v_lshl_add_u32 v3, s12, 13, v0
	s_add_u32 s12, s56, 0x45c00000
	v_lshl_add_u32 v0, s13, 12, v0
	s_addc_u32 s13, s57, 0
	s_ashr_i32 s48, s2, 31
	s_add_u32 s14, s26, 0x80
	s_waitcnt vmcnt(2)
	s_barrier
	s_addc_u32 s15, s27, 0
	s_add_i32 s49, s34, 0x18000
	s_mov_b32 m0, s49
	s_nop 0
	global_load_lds_dwordx4 v134, s[14:15]
	s_add_i32 s50, s34, 0x1a000
	s_mov_b32 m0, s50
	s_nop 0
	global_load_lds_dwordx4 v138, s[14:15]
	s_add_u32 s14, s28, 0x80
	s_addc_u32 s15, s29, 0
	s_add_i32 s51, s34, 0x8000
	s_mov_b32 m0, s51
	s_nop 0
	global_load_lds_dwordx4 v132, s[14:15]
	s_add_i32 s52, s34, 0xa000
	v_and_b32_e32 v133, 15, v7
	v_ashrrev_i32_e32 v4, 1, v7
	v_and_b32_e32 v1, 48, v7
	v_lshlrev_b32_e32 v5, 2, v7
	s_mov_b32 m0, s52
	s_nop 0
	global_load_lds_dwordx4 v136, s[14:15]
	s_add_u32 s4, s4, 0x80
	v_and_b32_e32 v2, -8, v4
	v_lshl_or_b32 v1, v133, 6, v1
	v_and_b32_e32 v5, 32, v5
	s_addc_u32 s5, s5, 0
	s_add_i32 s53, s34, 0x1c000
	s_mov_b32 m0, s53
	s_nop 0
	global_load_lds_dwordx4 v134, s[4:5]
	s_add_i32 s54, s34, 0x1e000
	v_bitop3_b32 v6, v1, v3, v5 bitop3:0xde
	s_mov_b32 m0, s54
	s_nop 0
	global_load_lds_dwordx4 v138, s[4:5]
	s_cmpk_gt_i32 s0, 0x7f
	v_add_u32_e32 v135, s1, v2
	v_ashrrev_i32_e32 v3, 31, v2
	v_bitop3_b32 v5, v1, v0, v5 bitop3:0xde
	s_waitcnt vmcnt(6)
	s_cselect_b64 s[14:15], -1, 0
	s_add_i32 s55, s46, -2
	s_add_i32 s64, s34, 0xc000
	v_add_u32_e32 v137, s1, v135
	v_lshl_add_u64 v[0:1], v[2:3], 2, s[56:57]
	s_mov_b64 s[0:1], 0x200000
	s_cmpk_lt_u32 s90, 0x100
	v_lshl_add_u64 v[140:141], v[0:1], 0, s[0:1]
	v_and_b32_e32 v0, 56, v4
	v_add_u32_e32 v1, 0, v5
	s_cselect_b64 s[16:17], -1, 0
	v_mov_b32_e32 v143, 0
	s_add_i32 s65, s34, 0xe000
	v_and_b32_e32 v144, 56, v135
	s_ashr_i32 s66, s76, 31
	v_mov_b64_e32 v[146:147], 0x600
	v_mov_b64_e32 v[148:149], 0x5ff
	s_movk_i32 s67, 0xc1
	v_add_u32_e32 v139, 0x10000, v1
	v_add_u32_e32 v164, 0x14000, v1
	v_add_u32_e32 v165, 0, v6
	v_add_u32_e32 v166, 0x18000, v1
	v_add_u32_e32 v167, 0x1c000, v1
	s_movk_i32 s68, 0x5ff
	s_mov_b32 s69, 0xaaaaaaab
	s_movk_i32 s70, 0x600
	s_movk_i32 s71, 0x300
	s_movk_i32 s72, 0x57f
	v_lshlrev_b32_e32 v150, 1, v0
	s_mov_b64 s[18:19], 0x1000
	s_movk_i32 s73, 0x1000
	s_mov_b64 s[20:21], 0x1800
	v_mov_b32_e32 v168, 0x3e38aa3b
	v_mov_b32_e32 v169, 0x600
	s_barrier
	s_mov_b32 s101, 0
	s_branch .LBB0_216

; #define PG8_BAR __builtin_amdgcn_s_barrier()
; template <class Epi, class Sched, bool ALIGN_EPI, bool FP8 = false>
; __device__ __forceinline__ void gemm_phase(PG8_LAS unsigned char* lds, const Gemm g, const Sched& S, const Epi& E, const int wid, const int lane) {
;     ...
;         if (!has_next) break;
; #pragma unroll
;         for (int a = 0; a < 2; ++a)
; #pragma unroll
;             for (int b = 0; b < 2; ++b)
; #pragma unroll
;                 for (int m = 0; m < 4; ++m)
; #pragma unroll
;                     for (int n = 0; n < 2; ++n) acc[a][b][m][n] = (f32x4){0.f, 0.f, 0.f, 0.f};
;         cur = nxt; cA = nA; cB = nB; ++ui;
;         if constexpr (ALIGN_EPI) { if (wr == 1) PG8_BAR; }
.LBB0_215:
	s_mov_b32 s101, 1
	s_andn2_b64 vcc, exec, s[0:1]
	s_mov_b32 s82, s74
	s_mov_b32 s83, s75
	s_mov_b64 s[26:27], s[24:25]
	s_mov_b64 s[28:29], s[22:23]
	s_cbranch_vccz .LBB0_298

; #define PG8_STAGE(bufoff, gbase, voff) do { _Pragma("unroll") for (int _i = 0; _i < 2; ++_i) { unsigned keep_; \
;         asm volatile("s_mov_b32 %0, m0\n\ts_mov_b32 m0, %3\n\ts_nop 0\n\tglobal_load_lds_dwordx4 %1, %2\n\ts_mov_b32 m0, %0" : "=&s"(keep_) : "v"((voff)[_i]), "s"((const char*)(gbase)), "s"(ldsb + (unsigned)((bufoff) + _i * 8192)) : "memory"); } } while (0)
; #define PG8_LDA(dst, b, h) do { _Pragma("unroll") for (int m = 0; m < 4; ++m) _Pragma("unroll") for (int k = 0; k < 2; ++k) dst[m][k] = *(const PG8_LAS bf16x8*)(lds + PG8_SA(b, h) + aoff + m * 2048 + k * 1024); } while (0)
; #define PG8_LDB(dst, b, h) do { _Pragma("unroll") for (int n = 0; n < 2; ++n) _Pragma("unroll") for (int k = 0; k < 2; ++k) dst[n][k] = *(const PG8_LAS bf16x8*)(lds + PG8_SB(b, h) + boff + n * 2048 + k * 1024); } while (0)
; #define PG8_WAIT_V(n) asm volatile("s_waitcnt vmcnt(" #n ")" ::: "memory")
; #define PG8_WAIT_L(n) asm volatile("s_waitcnt lgkmcnt(" #n ")" ::: "memory")
; #define PG8_BAR __builtin_amdgcn_s_barrier()
; #define PG8_SCHED __builtin_amdgcn_sched_barrier(0)
; template <class Epi, class Sched, bool ALIGN_EPI, bool FP8 = false>
; __device__ __forceinline__ void gemm_phase(PG8_LAS unsigned char* lds, const Gemm g, const Sched& S, const Epi& E, const int wid, const int lane) {
;     ...
;             PG8_LDB(B0, 0, 0); PG8_LDB(B1, 0, 1); PG8_SCHED; PG8_LDA(At, 0, 0); PG8_STAGE(PG8_SA(1, 1), a1 + hstepA, vc1);
;             if (GA && last && has_next) { const u32x4 q = *gslot; vc0[0] = q.x; vc0[1] = q.y; vc1[0] = q.z; vc1[1] = q.w; }
;             PG8_WAIT_V(8); PG8_WAIT_L(0); PG8_BAR; PG8_MMA(0, 0, At, B0); PG8_MMA(0, 1, At, B1); PG8_BAR; PG8_SCHED;
.LBB0_224:
	ds_read_b128 v[128:131], v139
	ds_read_b128 v[152:155], v139 offset:1024
	ds_read_b128 v[156:159], v139 offset:2048
	ds_read_b128 v[160:163], v139 offset:3072
	ds_read_b128 v[170:173], v164
	ds_read_b128 v[174:177], v164 offset:1024
	ds_read_b128 v[178:181], v164 offset:2048
	ds_read_b128 v[182:185], v164 offset:3072
	s_add_i32 s33, s26, 2
	s_cmp_eq_u32 s55, s26
	s_cselect_b32 s30, s22, s60
	s_cselect_b32 s31, s23, s61
	s_cselect_b32 s28, s24, s62
	s_cselect_b32 s29, s25, s63
	s_add_u32 s26, s30, 0x80
	s_addc_u32 s27, s31, 0
	ds_read_b128 v[186:189], v165
	ds_read_b128 v[190:193], v165 offset:1024
	ds_read_b128 v[194:197], v165 offset:2048
	ds_read_b128 v[198:201], v165 offset:3072
	ds_read_b128 v[202:205], v165 offset:4096
	ds_read_b128 v[206:209], v165 offset:5120
	ds_read_b128 v[210:213], v165 offset:6144
	ds_read_b128 v[218:221], v165 offset:7168
	s_mov_b32 m0, s64
	s_nop 0
	global_load_lds_dwordx4 v132, s[4:5]
	s_mov_b32 m0, s65
	s_nop 0
	global_load_lds_dwordx4 v136, s[4:5]
	s_cmp_eq_u32 s101, 0
	s_cbranch_scc1 .Lrxn2_0
	s_waitcnt vmcnt(24)
	s_branch .Lrxj2_0

; #define PG8_STAGE(bufoff, gbase, voff) do { _Pragma("unroll") for (int _i = 0; _i < 2; ++_i) { unsigned keep_; \
;         asm volatile("s_mov_b32 %0, m0\n\ts_mov_b32 m0, %3\n\ts_nop 0\n\tglobal_load_lds_dwordx4 %1, %2\n\ts_mov_b32 m0, %0" : "=&s"(keep_) : "v"((voff)[_i]), "s"((const char*)(gbase)), "s"(ldsb + (unsigned)((bufoff) + _i * 8192)) : "memory"); } } while (0)
; #define PG8_LDA(dst, b, h) do { _Pragma("unroll") for (int m = 0; m < 4; ++m) _Pragma("unroll") for (int k = 0; k < 2; ++k) dst[m][k] = *(const PG8_LAS bf16x8*)(lds + PG8_SA(b, h) + aoff + m * 2048 + k * 1024); } while (0)
; #define PG8_WAIT_V(n) asm volatile("s_waitcnt vmcnt(" #n ")" ::: "memory")
; #define PG8_WAIT_L(n) asm volatile("s_waitcnt lgkmcnt(" #n ")" ::: "memory")
; #define PG8_BAR __builtin_amdgcn_s_barrier()
; #define PG8_SCHED __builtin_amdgcn_sched_barrier(0)
; template <class Epi, class Sched, bool ALIGN_EPI, bool FP8 = false>
; __device__ __forceinline__ void gemm_phase(PG8_LAS unsigned char* lds, const Gemm g, const Sched& S, const Epi& E, const int wid, const int lane) {
;     ...
;             PG8_WAIT_V(8); PG8_WAIT_L(0); PG8_BAR; PG8_MMA(0, 0, At, B0); PG8_MMA(0, 1, At, B1); PG8_BAR; PG8_SCHED;
;             PG8_LDA(At, 0, 1); PG8_STAGE(PG8_SB(0, 0), b2, voffB); PG8_STAGE(PG8_SB(0, 1), b2 + hstep, voffB); PG8_STAGE(PG8_SA(0, 0), a2, vc0);
.Lrxj2_0:
	s_waitcnt lgkmcnt(0)
	s_barrier
	s_setprio 1
	s_waitcnt lgkmcnt(7)
	v_mfma_f32_16x16x32_bf16 v[124:127], v[128:131], v[186:189], v[124:127]
	v_mfma_f32_16x16x32_bf16 v[120:123], v[156:159], v[186:189], v[120:123]
	s_waitcnt lgkmcnt(5)
	v_mfma_f32_16x16x32_bf16 v[108:111], v[128:131], v[194:197], v[108:111]
	v_mfma_f32_16x16x32_bf16 v[104:107], v[156:159], v[194:197], v[104:107]
	s_waitcnt lgkmcnt(3)
	v_mfma_f32_16x16x32_bf16 v[92:95], v[128:131], v[202:205], v[92:95]
	v_mfma_f32_16x16x32_bf16 v[88:91], v[156:159], v[202:205], v[88:91]
	s_waitcnt lgkmcnt(1)
	v_mfma_f32_16x16x32_bf16 v[76:79], v[128:131], v[210:213], v[76:79]
	v_mfma_f32_16x16x32_bf16 v[72:75], v[156:159], v[210:213], v[72:75]
	v_mfma_f32_16x16x32_bf16 v[124:127], v[152:155], v[190:193], v[124:127]
	v_mfma_f32_16x16x32_bf16 v[120:123], v[160:163], v[190:193], v[120:123]
	v_mfma_f32_16x16x32_bf16 v[108:111], v[152:155], v[198:201], v[108:111]
	v_mfma_f32_16x16x32_bf16 v[104:107], v[160:163], v[198:201], v[104:107]
	v_mfma_f32_16x16x32_bf16 v[92:95], v[152:155], v[206:209], v[92:95]
	v_mfma_f32_16x16x32_bf16 v[88:91], v[160:163], v[206:209], v[88:91]
	s_waitcnt lgkmcnt(0)
	v_mfma_f32_16x16x32_bf16 v[76:79], v[152:155], v[218:221], v[76:79]
	v_mfma_f32_16x16x32_bf16 v[72:75], v[160:163], v[218:221], v[72:75]
	s_setprio 0
	s_setprio 1
	v_mfma_f32_16x16x32_bf16 v[116:119], v[170:173], v[186:189], v[116:119]
	v_mfma_f32_16x16x32_bf16 v[112:115], v[178:181], v[186:189], v[112:115]
	v_mfma_f32_16x16x32_bf16 v[100:103], v[170:173], v[194:197], v[100:103]
	v_mfma_f32_16x16x32_bf16 v[96:99], v[178:181], v[194:197], v[96:99]
	v_mfma_f32_16x16x32_bf16 v[84:87], v[170:173], v[202:205], v[84:87]
	v_mfma_f32_16x16x32_bf16 v[80:83], v[178:181], v[202:205], v[80:83]
	v_mfma_f32_16x16x32_bf16 v[68:71], v[170:173], v[210:213], v[68:71]
	v_mfma_f32_16x16x32_bf16 v[64:67], v[178:181], v[210:213], v[64:67]
	v_mfma_f32_16x16x32_bf16 v[116:119], v[174:177], v[190:193], v[116:119]
	v_mfma_f32_16x16x32_bf16 v[112:115], v[182:185], v[190:193], v[112:115]
	v_mfma_f32_16x16x32_bf16 v[100:103], v[174:177], v[198:201], v[100:103]
	v_mfma_f32_16x16x32_bf16 v[96:99], v[182:185], v[198:201], v[96:99]
	v_mfma_f32_16x16x32_bf16 v[84:87], v[174:177], v[206:209], v[84:87]
	v_mfma_f32_16x16x32_bf16 v[80:83], v[182:185], v[206:209], v[80:83]
	v_mfma_f32_16x16x32_bf16 v[68:71], v[174:177], v[218:221], v[68:71]
	v_mfma_f32_16x16x32_bf16 v[64:67], v[182:185], v[218:221], v[64:67]
	s_setprio 0
	s_barrier
	ds_read_b128 v[186:189], v165 offset:16384
	ds_read_b128 v[190:193], v165 offset:17408
	ds_read_b128 v[194:197], v165 offset:18432
	ds_read_b128 v[198:201], v165 offset:19456
	ds_read_b128 v[202:205], v165 offset:20480
	ds_read_b128 v[206:209], v165 offset:21504
	ds_read_b128 v[210:213], v165 offset:22528
	ds_read_b128 v[218:221], v165 offset:23552
	s_mov_b32 m0, s39
	s_nop 0
	global_load_lds_dwordx4 v134, s[28:29]
	s_mov_b32 m0, s40
	s_nop 0
	global_load_lds_dwordx4 v138, s[28:29]
	s_add_u32 s58, s28, s6
	s_addc_u32 s59, s29, s7
	s_mov_b32 m0, s41
	s_nop 0
	global_load_lds_dwordx4 v134, s[58:59]
	s_mov_b32 m0, s42
	s_nop 0
	global_load_lds_dwordx4 v138, s[58:59]
	s_mov_b32 m0, s34
	s_nop 0
	global_load_lds_dwordx4 v132, s[30:31]
	s_mov_b32 m0, s43
	s_nop 0
	global_load_lds_dwordx4 v136, s[30:31]
	s_cmp_eq_u32 s101, 0
	s_cbranch_scc1 .Lrxn2_1
	s_waitcnt vmcnt(24)
	s_branch .Lrxj2_1

; #define PG8_STAGE(bufoff, gbase, voff) do { _Pragma("unroll") for (int _i = 0; _i < 2; ++_i) { unsigned keep_; \
;         asm volatile("s_mov_b32 %0, m0\n\ts_mov_b32 m0, %3\n\ts_nop 0\n\tglobal_load_lds_dwordx4 %1, %2\n\ts_mov_b32 m0, %0" : "=&s"(keep_) : "v"((voff)[_i]), "s"((const char*)(gbase)), "s"(ldsb + (unsigned)((bufoff) + _i * 8192)) : "memory"); } } while (0)
; #define PG8_LDA(dst, b, h) do { _Pragma("unroll") for (int m = 0; m < 4; ++m) _Pragma("unroll") for (int k = 0; k < 2; ++k) dst[m][k] = *(const PG8_LAS bf16x8*)(lds + PG8_SA(b, h) + aoff + m * 2048 + k * 1024); } while (0)
; #define PG8_LDB(dst, b, h) do { _Pragma("unroll") for (int n = 0; n < 2; ++n) _Pragma("unroll") for (int k = 0; k < 2; ++k) dst[n][k] = *(const PG8_LAS bf16x8*)(lds + PG8_SB(b, h) + boff + n * 2048 + k * 1024); } while (0)
; #define PG8_WAIT_V(n) asm volatile("s_waitcnt vmcnt(" #n ")" ::: "memory")
; #define PG8_WAIT_L(n) asm volatile("s_waitcnt lgkmcnt(" #n ")" ::: "memory")
; #define PG8_BAR __builtin_amdgcn_s_barrier()
; #define PG8_SCHED __builtin_amdgcn_sched_barrier(0)
; template <class Epi, class Sched, bool ALIGN_EPI, bool FP8 = false>
; __device__ __forceinline__ void gemm_phase(PG8_LAS unsigned char* lds, const Gemm g, const Sched& S, const Epi& E, const int wid, const int lane) {
;     ...
;             PG8_WAIT_V(8); PG8_WAIT_L(0); PG8_BAR; PG8_MMA(1, 0, At, B0); PG8_MMA(1, 1, At, B1); PG8_BAR; PG8_SCHED;
;             PG8_LDB(B0, 1, 0); PG8_LDB(B1, 1, 1); PG8_SCHED; PG8_LDA(At, 1, 0); PG8_STAGE(PG8_SA(0, 1), a2 + hstepA, vc1);
;             PG8_WAIT_V(8); PG8_WAIT_L(0); PG8_BAR; PG8_MMA(0, 0, At, B0); PG8_MMA(0, 1, At, B1); PG8_BAR; PG8_SCHED;
.Lrxj2_1:
	s_mov_b32 s101, 0
	s_waitcnt lgkmcnt(0)
	s_barrier
	s_setprio 1
	s_waitcnt lgkmcnt(7)
	v_mfma_f32_16x16x32_bf16 v[60:63], v[128:131], v[186:189], v[60:63]
	v_mfma_f32_16x16x32_bf16 v[56:59], v[156:159], v[186:189], v[56:59]
	s_waitcnt lgkmcnt(5)
	v_mfma_f32_16x16x32_bf16 v[44:47], v[128:131], v[194:197], v[44:47]
	v_mfma_f32_16x16x32_bf16 v[40:43], v[156:159], v[194:197], v[40:43]
	s_waitcnt lgkmcnt(3)
	v_mfma_f32_16x16x32_bf16 v[28:31], v[128:131], v[202:205], v[28:31]
	v_mfma_f32_16x16x32_bf16 v[24:27], v[156:159], v[202:205], v[24:27]
	s_waitcnt lgkmcnt(1)
	v_mfma_f32_16x16x32_bf16 v[12:15], v[128:131], v[210:213], v[12:15]
	v_mfma_f32_16x16x32_bf16 v[8:11], v[156:159], v[210:213], v[8:11]
	v_mfma_f32_16x16x32_bf16 v[60:63], v[152:155], v[190:193], v[60:63]
	v_mfma_f32_16x16x32_bf16 v[56:59], v[160:163], v[190:193], v[56:59]
	v_mfma_f32_16x16x32_bf16 v[44:47], v[152:155], v[198:201], v[44:47]
	v_mfma_f32_16x16x32_bf16 v[40:43], v[160:163], v[198:201], v[40:43]
	v_mfma_f32_16x16x32_bf16 v[28:31], v[152:155], v[206:209], v[28:31]
	v_mfma_f32_16x16x32_bf16 v[24:27], v[160:163], v[206:209], v[24:27]
	s_waitcnt lgkmcnt(0)
	v_mfma_f32_16x16x32_bf16 v[12:15], v[152:155], v[218:221], v[12:15]
	v_mfma_f32_16x16x32_bf16 v[8:11], v[160:163], v[218:221], v[8:11]
	s_setprio 0
	s_setprio 1
	v_mfma_f32_16x16x32_bf16 v[52:55], v[170:173], v[186:189], v[52:55]
	v_mfma_f32_16x16x32_bf16 v[48:51], v[178:181], v[186:189], v[48:51]
	v_mfma_f32_16x16x32_bf16 v[36:39], v[170:173], v[194:197], v[36:39]
	v_mfma_f32_16x16x32_bf16 v[32:35], v[178:181], v[194:197], v[32:35]
	v_mfma_f32_16x16x32_bf16 v[20:23], v[170:173], v[202:205], v[20:23]
	v_mfma_f32_16x16x32_bf16 v[16:19], v[178:181], v[202:205], v[16:19]
	v_mfma_f32_16x16x32_bf16 v[4:7], v[170:173], v[210:213], v[4:7]
	v_mfma_f32_16x16x32_bf16 v[0:3], v[178:181], v[210:213], v[0:3]
	v_mfma_f32_16x16x32_bf16 v[52:55], v[174:177], v[190:193], v[52:55]
	v_mfma_f32_16x16x32_bf16 v[48:51], v[182:185], v[190:193], v[48:51]
	v_mfma_f32_16x16x32_bf16 v[36:39], v[174:177], v[198:201], v[36:39]
	v_mfma_f32_16x16x32_bf16 v[32:35], v[182:185], v[198:201], v[32:35]
	v_mfma_f32_16x16x32_bf16 v[20:23], v[174:177], v[206:209], v[20:23]
	v_mfma_f32_16x16x32_bf16 v[16:19], v[182:185], v[206:209], v[16:19]
	v_mfma_f32_16x16x32_bf16 v[4:7], v[174:177], v[218:221], v[4:7]
	v_mfma_f32_16x16x32_bf16 v[0:3], v[182:185], v[218:221], v[0:3]
	s_setprio 0
	s_barrier
	ds_read_b128 v[128:131], v166
	ds_read_b128 v[152:155], v166 offset:1024
	ds_read_b128 v[156:159], v166 offset:2048
	ds_read_b128 v[160:163], v166 offset:3072
	ds_read_b128 v[170:173], v167
	ds_read_b128 v[174:177], v167 offset:1024
	ds_read_b128 v[178:181], v167 offset:2048
	ds_read_b128 v[182:185], v167 offset:3072
	ds_read_b128 v[186:189], v165 offset:32768
	ds_read_b128 v[190:193], v165 offset:33792
	ds_read_b128 v[194:197], v165 offset:34816
	ds_read_b128 v[198:201], v165 offset:35840
	ds_read_b128 v[202:205], v165 offset:36864
	ds_read_b128 v[206:209], v165 offset:37888
	ds_read_b128 v[210:213], v165 offset:38912
	ds_read_b128 v[218:221], v165 offset:39936
	s_add_u32 s30, s30, s6
	s_addc_u32 s31, s31, s7
	s_mov_b32 m0, s44
	s_nop 0
	global_load_lds_dwordx4 v132, s[30:31]
	s_mov_b32 m0, s45
	s_nop 0
	global_load_lds_dwordx4 v136, s[30:31]
	s_waitcnt vmcnt(8)
	s_waitcnt lgkmcnt(0)
	s_barrier
	s_setprio 1
	s_waitcnt lgkmcnt(7)
	v_mfma_f32_16x16x32_bf16 v[124:127], v[128:131], v[186:189], v[124:127]
	v_mfma_f32_16x16x32_bf16 v[120:123], v[156:159], v[186:189], v[120:123]
	s_waitcnt lgkmcnt(5)
	v_mfma_f32_16x16x32_bf16 v[108:111], v[128:131], v[194:197], v[108:111]
	v_mfma_f32_16x16x32_bf16 v[104:107], v[156:159], v[194:197], v[104:107]
	s_waitcnt lgkmcnt(3)
	v_mfma_f32_16x16x32_bf16 v[92:95], v[128:131], v[202:205], v[92:95]
	v_mfma_f32_16x16x32_bf16 v[88:91], v[156:159], v[202:205], v[88:91]
	s_waitcnt lgkmcnt(1)
	v_mfma_f32_16x16x32_bf16 v[76:79], v[128:131], v[210:213], v[76:79]
	v_mfma_f32_16x16x32_bf16 v[72:75], v[156:159], v[210:213], v[72:75]
	v_mfma_f32_16x16x32_bf16 v[124:127], v[152:155], v[190:193], v[124:127]
	v_mfma_f32_16x16x32_bf16 v[120:123], v[160:163], v[190:193], v[120:123]
	v_mfma_f32_16x16x32_bf16 v[108:111], v[152:155], v[198:201], v[108:111]
	v_mfma_f32_16x16x32_bf16 v[104:107], v[160:163], v[198:201], v[104:107]
	v_mfma_f32_16x16x32_bf16 v[92:95], v[152:155], v[206:209], v[92:95]
	v_mfma_f32_16x16x32_bf16 v[88:91], v[160:163], v[206:209], v[88:91]
	s_waitcnt lgkmcnt(0)
	v_mfma_f32_16x16x32_bf16 v[76:79], v[152:155], v[218:221], v[76:79]
	v_mfma_f32_16x16x32_bf16 v[72:75], v[160:163], v[218:221], v[72:75]
	s_setprio 0
	s_setprio 1
	v_mfma_f32_16x16x32_bf16 v[116:119], v[170:173], v[186:189], v[116:119]
	v_mfma_f32_16x16x32_bf16 v[112:115], v[178:181], v[186:189], v[112:115]
	v_mfma_f32_16x16x32_bf16 v[100:103], v[170:173], v[194:197], v[100:103]
	v_mfma_f32_16x16x32_bf16 v[96:99], v[178:181], v[194:197], v[96:99]
	v_mfma_f32_16x16x32_bf16 v[84:87], v[170:173], v[202:205], v[84:87]
	v_mfma_f32_16x16x32_bf16 v[80:83], v[178:181], v[202:205], v[80:83]
	v_mfma_f32_16x16x32_bf16 v[68:71], v[170:173], v[210:213], v[68:71]
	v_mfma_f32_16x16x32_bf16 v[64:67], v[178:181], v[210:213], v[64:67]
	v_mfma_f32_16x16x32_bf16 v[116:119], v[174:177], v[190:193], v[116:119]
	v_mfma_f32_16x16x32_bf16 v[112:115], v[182:185], v[190:193], v[112:115]
	v_mfma_f32_16x16x32_bf16 v[100:103], v[174:177], v[198:201], v[100:103]
	v_mfma_f32_16x16x32_bf16 v[96:99], v[182:185], v[198:201], v[96:99]
	v_mfma_f32_16x16x32_bf16 v[84:87], v[174:177], v[206:209], v[84:87]
	v_mfma_f32_16x16x32_bf16 v[80:83], v[182:185], v[206:209], v[80:83]
	v_mfma_f32_16x16x32_bf16 v[68:71], v[174:177], v[218:221], v[68:71]
	v_mfma_f32_16x16x32_bf16 v[64:67], v[182:185], v[218:221], v[64:67]
	s_setprio 0
	s_barrier
; #define PG8_STAGE(bufoff, gbase, voff) do { _Pragma("unroll") for (int _i = 0; _i < 2; ++_i) { unsigned keep_; \
;         asm volatile("s_mov_b32 %0, m0\n\ts_mov_b32 m0, %3\n\ts_nop 0\n\tglobal_load_lds_dwordx4 %1, %2\n\ts_mov_b32 m0, %0" : "=&s"(keep_) : "v"((voff)[_i]), "s"((const char*)(gbase)), "s"(ldsb + (unsigned)((bufoff) + _i * 8192)) : "memory"); } } while (0)
; #define PG8_LDA(dst, b, h) do { _Pragma("unroll") for (int m = 0; m < 4; ++m) _Pragma("unroll") for (int k = 0; k < 2; ++k) dst[m][k] = *(const PG8_LAS bf16x8*)(lds + PG8_SA(b, h) + aoff + m * 2048 + k * 1024); } while (0)
; #define PG8_WAIT_V(n) asm volatile("s_waitcnt vmcnt(" #n ")" ::: "memory")
; #define PG8_WAIT_L(n) asm volatile("s_waitcnt lgkmcnt(" #n ")" ::: "memory")
; #define PG8_BAR __builtin_amdgcn_s_barrier()
; #define PG8_SCHED __builtin_amdgcn_sched_barrier(0)
; template <class Epi, class Sched, bool ALIGN_EPI, bool FP8 = false>
; __device__ __forceinline__ void gemm_phase(PG8_LAS unsigned char* lds, const Gemm g, const Sched& S, const Epi& E, const int wid, const int lane) {
;     ...
;             PG8_LDA(At, 1, 1); PG8_STAGE(PG8_SB(1, 0), b3, voffB); PG8_STAGE(PG8_SB(1, 1), b3 + hstep, voffB); PG8_STAGE(PG8_SA(1, 0), a3, vc0);
;             PG8_WAIT_V(8); PG8_WAIT_L(0); PG8_BAR; PG8_MMA(1, 0, At, B0); PG8_MMA(1, 1, At, B1); PG8_BAR; PG8_SCHED;
;         }
	ds_read_b128 v[186:189], v165 offset:49152
	ds_read_b128 v[190:193], v165 offset:50176
	ds_read_b128 v[194:197], v165 offset:51200
	ds_read_b128 v[198:201], v165 offset:52224
	ds_read_b128 v[202:205], v165 offset:53248
	ds_read_b128 v[206:209], v165 offset:54272
	ds_read_b128 v[210:213], v165 offset:55296
	ds_read_b128 v[218:221], v165 offset:56320
	s_add_u32 s28, s28, 0x80
	s_addc_u32 s29, s29, 0
	s_mov_b32 m0, s49
	s_nop 0
	global_load_lds_dwordx4 v134, s[28:29]
	s_mov_b32 m0, s50
	s_nop 0
	global_load_lds_dwordx4 v138, s[28:29]
	s_add_u32 s28, s28, s6
	s_addc_u32 s29, s29, s7
	s_mov_b32 m0, s53
	s_nop 0
	global_load_lds_dwordx4 v134, s[28:29]
	s_mov_b32 m0, s54
	s_nop 0
	global_load_lds_dwordx4 v138, s[28:29]
	s_mov_b32 m0, s51
	s_nop 0
	global_load_lds_dwordx4 v132, s[26:27]
	s_mov_b32 m0, s52
	s_nop 0
	global_load_lds_dwordx4 v136, s[26:27]
	s_waitcnt vmcnt(8)
	s_waitcnt lgkmcnt(0)
	s_barrier
	s_setprio 1
	s_waitcnt lgkmcnt(7)
	v_mfma_f32_16x16x32_bf16 v[60:63], v[128:131], v[186:189], v[60:63]
	v_mfma_f32_16x16x32_bf16 v[56:59], v[156:159], v[186:189], v[56:59]
	s_waitcnt lgkmcnt(5)
	v_mfma_f32_16x16x32_bf16 v[44:47], v[128:131], v[194:197], v[44:47]
	v_mfma_f32_16x16x32_bf16 v[40:43], v[156:159], v[194:197], v[40:43]
	s_waitcnt lgkmcnt(3)
	v_mfma_f32_16x16x32_bf16 v[28:31], v[128:131], v[202:205], v[28:31]
	v_mfma_f32_16x16x32_bf16 v[24:27], v[156:159], v[202:205], v[24:27]
	s_waitcnt lgkmcnt(1)
	v_mfma_f32_16x16x32_bf16 v[12:15], v[128:131], v[210:213], v[12:15]
	v_mfma_f32_16x16x32_bf16 v[8:11], v[156:159], v[210:213], v[8:11]
	v_mfma_f32_16x16x32_bf16 v[60:63], v[152:155], v[190:193], v[60:63]
	v_mfma_f32_16x16x32_bf16 v[56:59], v[160:163], v[190:193], v[56:59]
	v_mfma_f32_16x16x32_bf16 v[44:47], v[152:155], v[198:201], v[44:47]
	v_mfma_f32_16x16x32_bf16 v[40:43], v[160:163], v[198:201], v[40:43]
	v_mfma_f32_16x16x32_bf16 v[28:31], v[152:155], v[206:209], v[28:31]
	v_mfma_f32_16x16x32_bf16 v[24:27], v[160:163], v[206:209], v[24:27]
	s_waitcnt lgkmcnt(0)
	v_mfma_f32_16x16x32_bf16 v[12:15], v[152:155], v[218:221], v[12:15]
	v_mfma_f32_16x16x32_bf16 v[8:11], v[160:163], v[218:221], v[8:11]
	s_setprio 0
	s_setprio 1
	v_mfma_f32_16x16x32_bf16 v[52:55], v[170:173], v[186:189], v[52:55]
	v_mfma_f32_16x16x32_bf16 v[48:51], v[178:181], v[186:189], v[48:51]
	v_mfma_f32_16x16x32_bf16 v[36:39], v[170:173], v[194:197], v[36:39]
	v_mfma_f32_16x16x32_bf16 v[32:35], v[178:181], v[194:197], v[32:35]
	v_mfma_f32_16x16x32_bf16 v[20:23], v[170:173], v[202:205], v[20:23]
	v_mfma_f32_16x16x32_bf16 v[16:19], v[178:181], v[202:205], v[16:19]
	v_mfma_f32_16x16x32_bf16 v[4:7], v[170:173], v[210:213], v[4:7]
	v_mfma_f32_16x16x32_bf16 v[0:3], v[178:181], v[210:213], v[0:3]
	v_mfma_f32_16x16x32_bf16 v[52:55], v[174:177], v[190:193], v[52:55]
	v_mfma_f32_16x16x32_bf16 v[48:51], v[182:185], v[190:193], v[48:51]
	v_mfma_f32_16x16x32_bf16 v[36:39], v[174:177], v[198:201], v[36:39]
	v_mfma_f32_16x16x32_bf16 v[32:35], v[182:185], v[198:201], v[32:35]
	v_mfma_f32_16x16x32_bf16 v[20:23], v[174:177], v[206:209], v[20:23]
	v_mfma_f32_16x16x32_bf16 v[16:19], v[182:185], v[206:209], v[16:19]
	v_mfma_f32_16x16x32_bf16 v[4:7], v[174:177], v[218:221], v[4:7]
	v_mfma_f32_16x16x32_bf16 v[0:3], v[182:185], v[218:221], v[0:3]
	s_setprio 0
	s_barrier
	s_add_u32 s60, s60, 0x100
	s_addc_u32 s61, s61, 0
	s_add_u32 s62, s62, 0x100
	s_addc_u32 s63, s63, 0
	s_add_u32 s4, s4, 0x100
	s_addc_u32 s5, s5, 0
	s_cmp_ge_i32 s33, s46
	s_mov_b32 s26, s33
	s_cbranch_scc0 .LBB0_224

; #define PG8_STAGE(bufoff, gbase, voff) do { _Pragma("unroll") for (int _i = 0; _i < 2; ++_i) { unsigned keep_; \
;         asm volatile("s_mov_b32 %0, m0\n\ts_mov_b32 m0, %3\n\ts_nop 0\n\tglobal_load_lds_dwordx4 %1, %2\n\ts_mov_b32 m0, %0" : "=&s"(keep_) : "v"((voff)[_i]), "s"((const char*)(gbase)), "s"(ldsb + (unsigned)((bufoff) + _i * 8192)) : "memory"); } } while (0)
; #define PG8_WAIT_V(n) asm volatile("s_waitcnt vmcnt(" #n ")" ::: "memory")
; #define PG8_BAR __builtin_amdgcn_s_barrier()
; template <class Epi, class Sched, bool ALIGN_EPI, bool FP8 = false>
; __device__ __forceinline__ void gemm_phase(PG8_LAS unsigned char* lds, const Gemm g, const Sched& S, const Epi& E, const int wid, const int lane) {
;     ...
;     const int tid = wid * 64 + lane, wr = wid >> 2, wc = wid & 3, fr = lane & 15, fq = lane >> 4;
;     int KB = g.KB; asm volatile("" : "+s"(KB)); const int nt = KB / 128;
;     unsigned voffA[2], voffB[2]; int rA[2]; unsigned cA2[2];
; #pragma unroll
;     for (int i = 0; i < 2; ++i) { int R, C; stage_rc(tid * 16 + i * 8192, R, C); const int Rb = Epi::PERM ? ((R & ~31) + perm32(R & 31)) : R;
;         rA[i] = R; cA2[i] = (unsigned)C * 2u; voffA[i] = (unsigned)(R * KB + C * 2); voffB[i] = (unsigned)(Rb * KB + C * 2); }
;     const size_t kstep = (size_t)(BK * 2);
;     const size_t hstep = (size_t)HALF * KB;
;     const size_t hstepA = GA ? (size_t)0 : hstep;
;     const size_t tstep = 2 * hstep;
;     const unsigned ldsw = (unsigned)wid * 1024u;
;     const int aoff = lds_byte(wr * 64 + fr, fq * 8), boff = lds_byte(wc * 32 + fr, fq * 8);
;     ...
;     const char* cA = GA ? (const char*)g.A : (const char*)g.A + (size_t)cur.pm * tstep; const char* cB = (const char*)g.Bt + (size_t)cur.pn * tstep;
;     PG8_STAGE(PG8_SB(0, 0), cB, voffB); PG8_STAGE(PG8_SB(0, 1), cB + hstep, voffB); PG8_STAGE(PG8_SA(0, 0), cA, vc0); PG8_STAGE(PG8_SA(0, 1), cA + hstepA, vc1);
;     if (wr == 1) PG8_BAR;
;     PG8_WAIT_V(2); PG8_BAR;
;     PG8_STAGE(PG8_SB(1, 0), cB + kstep, voffB); PG8_STAGE(PG8_SA(1, 0), cA + kstep, vc0); PG8_STAGE(PG8_SB(1, 1), cB + hstep + kstep, voffB);
;     PG8_WAIT_V(6); PG8_BAR;
.LBB0_529:
	s_sext_i32_i8 s84, s12
	s_add_u32 s12, s56, 0x55c00000
	s_addc_u32 s13, s57, 0
	s_lshr_b32 s1, s1, 25
	s_add_i32 s1, s0, s1
	s_ashr_i32 s51, s1, 7
	v_ashrrev_i32_e32 v2, 6, v172
	s_lshl_b32 s1, s14, 13
	v_lshl_add_u32 v4, v2, 10, s1
	s_lshl_b32 s1, s80, 5
	v_and_b32_e32 v0, 15, v172
	s_and_b32 s1, s1, 0x60
	v_lshl_or_b32 v161, s14, 6, v0
	s_lshr_b32 s14, s1, 3
	v_add_lshl_u32 v2, v2, s14, 10
	s_add_u32 s14, s28, 0x80
	s_waitcnt vmcnt(2)
	s_barrier
	s_addc_u32 s15, s29, 0
	s_add_i32 s52, s42, 0x18000
	s_mov_b32 m0, s52
	s_nop 0
	global_load_lds_dwordx4 v162, s[14:15]
	s_add_i32 s53, s42, 0x1a000
	s_mov_b32 m0, s53
	s_nop 0
	global_load_lds_dwordx4 v166, s[14:15]
	s_add_u32 s14, s30, 0x80
	s_addc_u32 s15, s31, 0
	s_add_i32 s54, s42, 0x8000
	s_mov_b32 m0, s54
	s_nop 0
	global_load_lds_dwordx4 v160, s[14:15]
	s_add_i32 s55, s42, 0xa000
	v_and_b32_e32 v3, 48, v172
	s_mov_b32 m0, s55
	s_nop 0
	global_load_lds_dwordx4 v164, s[14:15]
	s_add_u32 s4, s4, 0x80
	v_lshl_or_b32 v0, v0, 6, v3
	v_lshlrev_b32_e32 v3, 2, v172
	s_addc_u32 s5, s5, 0
	s_add_i32 s64, s42, 0x1c000
	s_mov_b32 m0, s64
	s_nop 0
	global_load_lds_dwordx4 v162, s[4:5]
	s_add_i32 s65, s42, 0x1e000
	v_and_b32_e32 v3, 32, v3
	s_mov_b32 m0, s65
	s_nop 0
	global_load_lds_dwordx4 v166, s[4:5]
	s_cmpk_gt_i32 s0, 0x7f
	v_ashrrev_i32_e32 v1, 1, v172
	v_bitop3_b32 v4, v0, v4, v3 bitop3:0xde
	v_bitop3_b32 v0, v0, v2, v3 bitop3:0xde
	s_waitcnt vmcnt(6)
	s_cselect_b64 s[14:15], -1, 0
	s_add_i32 s66, s51, -2
	s_add_i32 s67, s42, 0xc000
	v_and_b32_e32 v1, -8, v1
	s_cmpk_lt_u32 s90, 0x100
	v_add_u32_e32 v0, 0, v0
	s_cselect_b64 s[16:17], -1, 0
	v_add_u32_e32 v163, s1, v1
	s_add_i32 s68, s42, 0xe000
	s_ashr_i32 s69, s76, 31
	v_mov_b64_e32 v[168:169], 0x200
	v_mov_b64_e32 v[170:171], 0x1ff
	v_add_u32_e32 v165, 0x10000, v0
	v_add_u32_e32 v167, 0x14000, v0
	v_add_u32_e32 v173, 0, v4
	v_mov_b32_e32 v174, 0x79
	v_mov_b32_e32 v175, 0x7b
	v_add_u32_e32 v176, 0x18000, v0
	v_add_u32_e32 v177, 0x1c000, v0
	s_mov_b64 s[18:19], 0x80000
	s_mov_b32 s70, 0x80000
	s_mov_b64 s[20:21], 0x90000
	s_mov_b32 s71, 0x90000
	s_mov_b64 s[22:23], 0xa0000
	s_mov_b32 s72, 0xa0000
	s_mov_b64 s[24:25], 0xb0000
	s_mov_b32 s73, 0xb0000
	s_barrier
	s_mov_b32 s101, 0
	s_branch .LBB0_532

; #define PG8_BAR __builtin_amdgcn_s_barrier()
; template <class Epi, class Sched, bool ALIGN_EPI, bool FP8 = false>
; __device__ __forceinline__ void gemm_phase(PG8_LAS unsigned char* lds, const Gemm g, const Sched& S, const Epi& E, const int wid, const int lane) {
;     ...
;         if (!has_next) break;
; #pragma unroll
;         for (int a = 0; a < 2; ++a)
; #pragma unroll
;             for (int b = 0; b < 2; ++b)
; #pragma unroll
;                 for (int m = 0; m < 4; ++m)
; #pragma unroll
;                     for (int n = 0; n < 2; ++n) acc[a][b][m][n] = (f32x4){0.f, 0.f, 0.f, 0.f};
;         cur = nxt; cA = nA; cB = nB; ++ui;
;         if constexpr (ALIGN_EPI) { if (wr == 1) PG8_BAR; }
.LBB0_531:
	s_mov_b32 s101, 1
	s_andn2_b64 vcc, exec, s[0:1]
	s_mov_b32 s84, s74
	s_mov_b32 s83, s75
	s_mov_b64 s[28:29], s[26:27]
	s_mov_b64 s[30:31], s[4:5]
	s_cbranch_vccz .LBB0_550

; #define PG8_STAGE(bufoff, gbase, voff) do { _Pragma("unroll") for (int _i = 0; _i < 2; ++_i) { unsigned keep_; \
;         asm volatile("s_mov_b32 %0, m0\n\ts_mov_b32 m0, %3\n\ts_nop 0\n\tglobal_load_lds_dwordx4 %1, %2\n\ts_mov_b32 m0, %0" : "=&s"(keep_) : "v"((voff)[_i]), "s"((const char*)(gbase)), "s"(ldsb + (unsigned)((bufoff) + _i * 8192)) : "memory"); } } while (0)
; #define PG8_LDA(dst, b, h) do { _Pragma("unroll") for (int m = 0; m < 4; ++m) _Pragma("unroll") for (int k = 0; k < 2; ++k) dst[m][k] = *(const PG8_LAS bf16x8*)(lds + PG8_SA(b, h) + aoff + m * 2048 + k * 1024); } while (0)
; #define PG8_LDB(dst, b, h) do { _Pragma("unroll") for (int n = 0; n < 2; ++n) _Pragma("unroll") for (int k = 0; k < 2; ++k) dst[n][k] = *(const PG8_LAS bf16x8*)(lds + PG8_SB(b, h) + boff + n * 2048 + k * 1024); } while (0)
; #define PG8_WAIT_V(n) asm volatile("s_waitcnt vmcnt(" #n ")" ::: "memory")
; #define PG8_WAIT_L(n) asm volatile("s_waitcnt lgkmcnt(" #n ")" ::: "memory")
; #define PG8_BAR __builtin_amdgcn_s_barrier()
; #define PG8_SCHED __builtin_amdgcn_sched_barrier(0)
; template <class Epi, class Sched, bool ALIGN_EPI, bool FP8 = false>
; __device__ __forceinline__ void gemm_phase(PG8_LAS unsigned char* lds, const Gemm g, const Sched& S, const Epi& E, const int wid, const int lane) {
;     ...
;             PG8_LDB(B0, 0, 0); PG8_LDB(B1, 0, 1); PG8_SCHED; PG8_LDA(At, 0, 0); PG8_STAGE(PG8_SA(1, 1), a1 + hstepA, vc1);
;             if (GA && last && has_next) { const u32x4 q = *gslot; vc0[0] = q.x; vc0[1] = q.y; vc1[0] = q.z; vc1[1] = q.w; }
;             PG8_WAIT_V(8); PG8_WAIT_L(0); PG8_BAR; PG8_MMA(0, 0, At, B0); PG8_MMA(0, 1, At, B1); PG8_BAR; PG8_SCHED;
.LBB0_544:
	ds_read_b128 v[24:27], v165
	ds_read_b128 v[28:31], v165 offset:1024
	ds_read_b128 v[16:19], v165 offset:2048
	ds_read_b128 v[20:23], v165 offset:3072
	ds_read_b128 v[8:11], v167
	ds_read_b128 v[12:15], v167 offset:1024
	ds_read_b128 v[0:3], v167 offset:2048
	ds_read_b128 v[4:7], v167 offset:3072
	s_add_i32 s33, s30, 2
	s_cmp_eq_u32 s66, s30
	s_cselect_b32 s36, s4, s82
	s_cselect_b32 s37, s5, s85
	s_cselect_b32 s34, s26, s86
	s_cselect_b32 s35, s27, s87
	s_add_u32 s30, s36, 0x80
	s_addc_u32 s31, s37, 0
	ds_read_b128 v[178:181], v173
	ds_read_b128 v[182:185], v173 offset:1024
	ds_read_b128 v[186:189], v173 offset:2048
	ds_read_b128 v[190:193], v173 offset:3072
	ds_read_b128 v[194:197], v173 offset:4096
	ds_read_b128 v[198:201], v173 offset:5120
	ds_read_b128 v[202:205], v173 offset:6144
	ds_read_b128 v[206:209], v173 offset:7168
	s_mov_b32 m0, s67
	s_nop 0
	global_load_lds_dwordx4 v160, s[28:29]
	s_mov_b32 m0, s68
	s_nop 0
	global_load_lds_dwordx4 v164, s[28:29]
	s_cmp_eq_u32 s101, 0
	s_cbranch_scc1 .Lrxn4_0
	s_waitcnt vmcnt(24)
	s_branch .Lrxj4_0

; #define PG8_STAGE(bufoff, gbase, voff) do { _Pragma("unroll") for (int _i = 0; _i < 2; ++_i) { unsigned keep_; \
;         asm volatile("s_mov_b32 %0, m0\n\ts_mov_b32 m0, %3\n\ts_nop 0\n\tglobal_load_lds_dwordx4 %1, %2\n\ts_mov_b32 m0, %0" : "=&s"(keep_) : "v"((voff)[_i]), "s"((const char*)(gbase)), "s"(ldsb + (unsigned)((bufoff) + _i * 8192)) : "memory"); } } while (0)
; #define PG8_LDA(dst, b, h) do { _Pragma("unroll") for (int m = 0; m < 4; ++m) _Pragma("unroll") for (int k = 0; k < 2; ++k) dst[m][k] = *(const PG8_LAS bf16x8*)(lds + PG8_SA(b, h) + aoff + m * 2048 + k * 1024); } while (0)
; #define PG8_WAIT_V(n) asm volatile("s_waitcnt vmcnt(" #n ")" ::: "memory")
; #define PG8_WAIT_L(n) asm volatile("s_waitcnt lgkmcnt(" #n ")" ::: "memory")
; #define PG8_BAR __builtin_amdgcn_s_barrier()
; #define PG8_SCHED __builtin_amdgcn_sched_barrier(0)
; template <class Epi, class Sched, bool ALIGN_EPI, bool FP8 = false>
; __device__ __forceinline__ void gemm_phase(PG8_LAS unsigned char* lds, const Gemm g, const Sched& S, const Epi& E, const int wid, const int lane) {
;     ...
;             PG8_WAIT_V(8); PG8_WAIT_L(0); PG8_BAR; PG8_MMA(0, 0, At, B0); PG8_MMA(0, 1, At, B1); PG8_BAR; PG8_SCHED;
;             PG8_LDA(At, 0, 1); PG8_STAGE(PG8_SB(0, 0), b2, voffB); PG8_STAGE(PG8_SB(0, 1), b2 + hstep, voffB); PG8_STAGE(PG8_SA(0, 0), a2, vc0);
.Lrxj4_0:
	s_waitcnt lgkmcnt(0)
	s_barrier
	s_setprio 1
	s_waitcnt lgkmcnt(6)
	v_mfma_scale_f32_16x16x128_f8f6f4 v[156:159], v[24:31], v[178:185], v[156:159], v174, v175 op_sel_hi:[0,0,0]
	v_mfma_scale_f32_16x16x128_f8f6f4 v[152:155], v[16:23], v[178:185], v[152:155], v174, v175 op_sel_hi:[0,0,0]
	s_waitcnt lgkmcnt(4)
	v_mfma_scale_f32_16x16x128_f8f6f4 v[140:143], v[24:31], v[186:193], v[140:143], v174, v175 op_sel_hi:[0,0,0]
	v_mfma_scale_f32_16x16x128_f8f6f4 v[136:139], v[16:23], v[186:193], v[136:139], v174, v175 op_sel_hi:[0,0,0]
	s_waitcnt lgkmcnt(2)
	v_mfma_scale_f32_16x16x128_f8f6f4 v[124:127], v[24:31], v[194:201], v[124:127], v174, v175 op_sel_hi:[0,0,0]
	v_mfma_scale_f32_16x16x128_f8f6f4 v[120:123], v[16:23], v[194:201], v[120:123], v174, v175 op_sel_hi:[0,0,0]
	s_waitcnt lgkmcnt(0)
	v_mfma_scale_f32_16x16x128_f8f6f4 v[108:111], v[24:31], v[202:209], v[108:111], v174, v175 op_sel_hi:[0,0,0]
	v_mfma_scale_f32_16x16x128_f8f6f4 v[104:107], v[16:23], v[202:209], v[104:107], v174, v175 op_sel_hi:[0,0,0]
	s_setprio 0
	s_setprio 1
	v_mfma_scale_f32_16x16x128_f8f6f4 v[148:151], v[8:15], v[178:185], v[148:151], v174, v175 op_sel_hi:[0,0,0]
	v_mfma_scale_f32_16x16x128_f8f6f4 v[144:147], v[0:7], v[178:185], v[144:147], v174, v175 op_sel_hi:[0,0,0]
	v_mfma_scale_f32_16x16x128_f8f6f4 v[132:135], v[8:15], v[186:193], v[132:135], v174, v175 op_sel_hi:[0,0,0]
	v_mfma_scale_f32_16x16x128_f8f6f4 v[128:131], v[0:7], v[186:193], v[128:131], v174, v175 op_sel_hi:[0,0,0]
	v_mfma_scale_f32_16x16x128_f8f6f4 v[116:119], v[8:15], v[194:201], v[116:119], v174, v175 op_sel_hi:[0,0,0]
	v_mfma_scale_f32_16x16x128_f8f6f4 v[112:115], v[0:7], v[194:201], v[112:115], v174, v175 op_sel_hi:[0,0,0]
	v_mfma_scale_f32_16x16x128_f8f6f4 v[100:103], v[8:15], v[202:209], v[100:103], v174, v175 op_sel_hi:[0,0,0]
	v_mfma_scale_f32_16x16x128_f8f6f4 v[96:99], v[0:7], v[202:209], v[96:99], v174, v175 op_sel_hi:[0,0,0]
	s_setprio 0
	s_barrier
	ds_read_b128 v[178:181], v173 offset:16384
	ds_read_b128 v[182:185], v173 offset:17408
	ds_read_b128 v[186:189], v173 offset:18432
	ds_read_b128 v[190:193], v173 offset:19456
	ds_read_b128 v[194:197], v173 offset:20480
	ds_read_b128 v[198:201], v173 offset:21504
	ds_read_b128 v[202:205], v173 offset:22528
	ds_read_b128 v[206:209], v173 offset:23552
	s_mov_b32 m0, s44
	s_nop 0
	global_load_lds_dwordx4 v162, s[34:35]
	s_mov_b32 m0, s45
	s_nop 0
	global_load_lds_dwordx4 v166, s[34:35]
	s_add_u32 s58, s34, s6
	s_addc_u32 s59, s35, s7
	s_mov_b32 m0, s46
	s_nop 0
	global_load_lds_dwordx4 v162, s[58:59]
	s_mov_b32 m0, s47
	s_nop 0
	global_load_lds_dwordx4 v166, s[58:59]
	s_mov_b32 m0, s42
	s_nop 0
	global_load_lds_dwordx4 v160, s[36:37]
	s_mov_b32 m0, s48
	s_nop 0
	global_load_lds_dwordx4 v164, s[36:37]
	s_cmp_eq_u32 s101, 0
	s_cbranch_scc1 .Lrxn4_1
	s_waitcnt vmcnt(24)
	s_branch .Lrxj4_1

; #define PG8_STAGE(bufoff, gbase, voff) do { _Pragma("unroll") for (int _i = 0; _i < 2; ++_i) { unsigned keep_; \
;         asm volatile("s_mov_b32 %0, m0\n\ts_mov_b32 m0, %3\n\ts_nop 0\n\tglobal_load_lds_dwordx4 %1, %2\n\ts_mov_b32 m0, %0" : "=&s"(keep_) : "v"((voff)[_i]), "s"((const char*)(gbase)), "s"(ldsb + (unsigned)((bufoff) + _i * 8192)) : "memory"); } } while (0)
; #define PG8_LDA(dst, b, h) do { _Pragma("unroll") for (int m = 0; m < 4; ++m) _Pragma("unroll") for (int k = 0; k < 2; ++k) dst[m][k] = *(const PG8_LAS bf16x8*)(lds + PG8_SA(b, h) + aoff + m * 2048 + k * 1024); } while (0)
; #define PG8_LDB(dst, b, h) do { _Pragma("unroll") for (int n = 0; n < 2; ++n) _Pragma("unroll") for (int k = 0; k < 2; ++k) dst[n][k] = *(const PG8_LAS bf16x8*)(lds + PG8_SB(b, h) + boff + n * 2048 + k * 1024); } while (0)
; #define PG8_WAIT_V(n) asm volatile("s_waitcnt vmcnt(" #n ")" ::: "memory")
; #define PG8_WAIT_L(n) asm volatile("s_waitcnt lgkmcnt(" #n ")" ::: "memory")
; #define PG8_BAR __builtin_amdgcn_s_barrier()
; #define PG8_SCHED __builtin_amdgcn_sched_barrier(0)
; template <class Epi, class Sched, bool ALIGN_EPI, bool FP8 = false>
; __device__ __forceinline__ void gemm_phase(PG8_LAS unsigned char* lds, const Gemm g, const Sched& S, const Epi& E, const int wid, const int lane) {
;     ...
;             PG8_WAIT_V(8); PG8_WAIT_L(0); PG8_BAR; PG8_MMA(1, 0, At, B0); PG8_MMA(1, 1, At, B1); PG8_BAR; PG8_SCHED;
;             PG8_LDB(B0, 1, 0); PG8_LDB(B1, 1, 1); PG8_SCHED; PG8_LDA(At, 1, 0); PG8_STAGE(PG8_SA(0, 1), a2 + hstepA, vc1);
;             PG8_WAIT_V(8); PG8_WAIT_L(0); PG8_BAR; PG8_MMA(0, 0, At, B0); PG8_MMA(0, 1, At, B1); PG8_BAR; PG8_SCHED;
.Lrxj4_1:
	s_mov_b32 s101, 0
	s_waitcnt lgkmcnt(0)
	s_barrier
	s_setprio 1
	s_waitcnt lgkmcnt(6)
	v_mfma_scale_f32_16x16x128_f8f6f4 v[92:95], v[24:31], v[178:185], v[92:95], v174, v175 op_sel_hi:[0,0,0]
	v_mfma_scale_f32_16x16x128_f8f6f4 v[88:91], v[16:23], v[178:185], v[88:91], v174, v175 op_sel_hi:[0,0,0]
	s_waitcnt lgkmcnt(4)
	v_mfma_scale_f32_16x16x128_f8f6f4 v[76:79], v[24:31], v[186:193], v[76:79], v174, v175 op_sel_hi:[0,0,0]
	v_mfma_scale_f32_16x16x128_f8f6f4 v[72:75], v[16:23], v[186:193], v[72:75], v174, v175 op_sel_hi:[0,0,0]
	s_waitcnt lgkmcnt(2)
	v_mfma_scale_f32_16x16x128_f8f6f4 v[60:63], v[24:31], v[194:201], v[60:63], v174, v175 op_sel_hi:[0,0,0]
	v_mfma_scale_f32_16x16x128_f8f6f4 v[56:59], v[16:23], v[194:201], v[56:59], v174, v175 op_sel_hi:[0,0,0]
	s_waitcnt lgkmcnt(0)
	v_mfma_scale_f32_16x16x128_f8f6f4 v[44:47], v[24:31], v[202:209], v[44:47], v174, v175 op_sel_hi:[0,0,0]
	v_mfma_scale_f32_16x16x128_f8f6f4 v[40:43], v[16:23], v[202:209], v[40:43], v174, v175 op_sel_hi:[0,0,0]
	s_setprio 0
	s_setprio 1
	v_mfma_scale_f32_16x16x128_f8f6f4 v[84:87], v[8:15], v[178:185], v[84:87], v174, v175 op_sel_hi:[0,0,0]
	v_mfma_scale_f32_16x16x128_f8f6f4 v[80:83], v[0:7], v[178:185], v[80:83], v174, v175 op_sel_hi:[0,0,0]
	v_mfma_scale_f32_16x16x128_f8f6f4 v[68:71], v[8:15], v[186:193], v[68:71], v174, v175 op_sel_hi:[0,0,0]
	v_mfma_scale_f32_16x16x128_f8f6f4 v[64:67], v[0:7], v[186:193], v[64:67], v174, v175 op_sel_hi:[0,0,0]
	v_mfma_scale_f32_16x16x128_f8f6f4 v[52:55], v[8:15], v[194:201], v[52:55], v174, v175 op_sel_hi:[0,0,0]
	v_mfma_scale_f32_16x16x128_f8f6f4 v[48:51], v[0:7], v[194:201], v[48:51], v174, v175 op_sel_hi:[0,0,0]
	v_mfma_scale_f32_16x16x128_f8f6f4 v[36:39], v[8:15], v[202:209], v[36:39], v174, v175 op_sel_hi:[0,0,0]
	v_mfma_scale_f32_16x16x128_f8f6f4 v[32:35], v[0:7], v[202:209], v[32:35], v174, v175 op_sel_hi:[0,0,0]
	s_setprio 0
	s_barrier
	ds_read_b128 v[0:3], v176
	ds_read_b128 v[4:7], v176 offset:1024
	ds_read_b128 v[8:11], v176 offset:2048
	ds_read_b128 v[12:15], v176 offset:3072
	ds_read_b128 v[16:19], v177
	ds_read_b128 v[20:23], v177 offset:1024
	ds_read_b128 v[24:27], v177 offset:2048
	ds_read_b128 v[28:31], v177 offset:3072
	ds_read_b128 v[178:181], v173 offset:32768
	ds_read_b128 v[182:185], v173 offset:33792
	ds_read_b128 v[186:189], v173 offset:34816
	ds_read_b128 v[190:193], v173 offset:35840
	ds_read_b128 v[194:197], v173 offset:36864
	ds_read_b128 v[198:201], v173 offset:37888
	ds_read_b128 v[202:205], v173 offset:38912
	ds_read_b128 v[206:209], v173 offset:39936
	s_add_u32 s36, s36, s6
	s_addc_u32 s37, s37, s7
	s_mov_b32 m0, s49
	s_nop 0
	global_load_lds_dwordx4 v160, s[36:37]
	s_mov_b32 m0, s50
	s_nop 0
	global_load_lds_dwordx4 v164, s[36:37]
	s_waitcnt vmcnt(8)
	s_waitcnt lgkmcnt(0)
	s_barrier
	s_setprio 1
	s_waitcnt lgkmcnt(6)
	v_mfma_scale_f32_16x16x128_f8f6f4 v[156:159], v[0:7], v[178:185], v[156:159], v174, v175 op_sel_hi:[0,0,0]
	v_mfma_scale_f32_16x16x128_f8f6f4 v[152:155], v[8:15], v[178:185], v[152:155], v174, v175 op_sel_hi:[0,0,0]
	s_waitcnt lgkmcnt(4)
	v_mfma_scale_f32_16x16x128_f8f6f4 v[140:143], v[0:7], v[186:193], v[140:143], v174, v175 op_sel_hi:[0,0,0]
	v_mfma_scale_f32_16x16x128_f8f6f4 v[136:139], v[8:15], v[186:193], v[136:139], v174, v175 op_sel_hi:[0,0,0]
	s_waitcnt lgkmcnt(2)
	v_mfma_scale_f32_16x16x128_f8f6f4 v[124:127], v[0:7], v[194:201], v[124:127], v174, v175 op_sel_hi:[0,0,0]
	v_mfma_scale_f32_16x16x128_f8f6f4 v[120:123], v[8:15], v[194:201], v[120:123], v174, v175 op_sel_hi:[0,0,0]
	s_waitcnt lgkmcnt(0)
	v_mfma_scale_f32_16x16x128_f8f6f4 v[108:111], v[0:7], v[202:209], v[108:111], v174, v175 op_sel_hi:[0,0,0]
	v_mfma_scale_f32_16x16x128_f8f6f4 v[104:107], v[8:15], v[202:209], v[104:107], v174, v175 op_sel_hi:[0,0,0]
	s_setprio 0
	s_setprio 1
	v_mfma_scale_f32_16x16x128_f8f6f4 v[148:151], v[16:23], v[178:185], v[148:151], v174, v175 op_sel_hi:[0,0,0]
	v_mfma_scale_f32_16x16x128_f8f6f4 v[144:147], v[24:31], v[178:185], v[144:147], v174, v175 op_sel_hi:[0,0,0]
	v_mfma_scale_f32_16x16x128_f8f6f4 v[132:135], v[16:23], v[186:193], v[132:135], v174, v175 op_sel_hi:[0,0,0]
	v_mfma_scale_f32_16x16x128_f8f6f4 v[128:131], v[24:31], v[186:193], v[128:131], v174, v175 op_sel_hi:[0,0,0]
	v_mfma_scale_f32_16x16x128_f8f6f4 v[116:119], v[16:23], v[194:201], v[116:119], v174, v175 op_sel_hi:[0,0,0]
	v_mfma_scale_f32_16x16x128_f8f6f4 v[112:115], v[24:31], v[194:201], v[112:115], v174, v175 op_sel_hi:[0,0,0]
	v_mfma_scale_f32_16x16x128_f8f6f4 v[100:103], v[16:23], v[202:209], v[100:103], v174, v175 op_sel_hi:[0,0,0]
	v_mfma_scale_f32_16x16x128_f8f6f4 v[96:99], v[24:31], v[202:209], v[96:99], v174, v175 op_sel_hi:[0,0,0]
	s_setprio 0
	s_barrier
; #define PG8_STAGE(bufoff, gbase, voff) do { _Pragma("unroll") for (int _i = 0; _i < 2; ++_i) { unsigned keep_; \
;         asm volatile("s_mov_b32 %0, m0\n\ts_mov_b32 m0, %3\n\ts_nop 0\n\tglobal_load_lds_dwordx4 %1, %2\n\ts_mov_b32 m0, %0" : "=&s"(keep_) : "v"((voff)[_i]), "s"((const char*)(gbase)), "s"(ldsb + (unsigned)((bufoff) + _i * 8192)) : "memory"); } } while (0)
; #define PG8_LDA(dst, b, h) do { _Pragma("unroll") for (int m = 0; m < 4; ++m) _Pragma("unroll") for (int k = 0; k < 2; ++k) dst[m][k] = *(const PG8_LAS bf16x8*)(lds + PG8_SA(b, h) + aoff + m * 2048 + k * 1024); } while (0)
; #define PG8_WAIT_V(n) asm volatile("s_waitcnt vmcnt(" #n ")" ::: "memory")
; #define PG8_WAIT_L(n) asm volatile("s_waitcnt lgkmcnt(" #n ")" ::: "memory")
; #define PG8_BAR __builtin_amdgcn_s_barrier()
; #define PG8_SCHED __builtin_amdgcn_sched_barrier(0)
; template <class Epi, class Sched, bool ALIGN_EPI, bool FP8 = false>
; __device__ __forceinline__ void gemm_phase(PG8_LAS unsigned char* lds, const Gemm g, const Sched& S, const Epi& E, const int wid, const int lane) {
;     ...
;             PG8_LDA(At, 1, 1); PG8_STAGE(PG8_SB(1, 0), b3, voffB); PG8_STAGE(PG8_SB(1, 1), b3 + hstep, voffB); PG8_STAGE(PG8_SA(1, 0), a3, vc0);
;             PG8_WAIT_V(8); PG8_WAIT_L(0); PG8_BAR; PG8_MMA(1, 0, At, B0); PG8_MMA(1, 1, At, B1); PG8_BAR; PG8_SCHED;
;         }
	ds_read_b128 v[178:181], v173 offset:49152
	ds_read_b128 v[182:185], v173 offset:50176
	ds_read_b128 v[186:189], v173 offset:51200
	ds_read_b128 v[190:193], v173 offset:52224
	ds_read_b128 v[194:197], v173 offset:53248
	ds_read_b128 v[198:201], v173 offset:54272
	ds_read_b128 v[202:205], v173 offset:55296
	ds_read_b128 v[206:209], v173 offset:56320
	s_add_u32 s34, s34, 0x80
	s_addc_u32 s35, s35, 0
	s_mov_b32 m0, s52
	s_nop 0
	global_load_lds_dwordx4 v162, s[34:35]
	s_mov_b32 m0, s53
	s_nop 0
	global_load_lds_dwordx4 v166, s[34:35]
	s_add_u32 s34, s34, s6
	s_addc_u32 s35, s35, s7
	s_mov_b32 m0, s64
	s_nop 0
	global_load_lds_dwordx4 v162, s[34:35]
	s_mov_b32 m0, s65
	s_nop 0
	global_load_lds_dwordx4 v166, s[34:35]
	s_mov_b32 m0, s54
	s_nop 0
	global_load_lds_dwordx4 v160, s[30:31]
	s_mov_b32 m0, s55
	s_nop 0
	global_load_lds_dwordx4 v164, s[30:31]
	s_waitcnt vmcnt(8)
	s_waitcnt lgkmcnt(0)
	s_barrier
	s_setprio 1
	s_waitcnt lgkmcnt(6)
	v_mfma_scale_f32_16x16x128_f8f6f4 v[92:95], v[0:7], v[178:185], v[92:95], v174, v175 op_sel_hi:[0,0,0]
	v_mfma_scale_f32_16x16x128_f8f6f4 v[88:91], v[8:15], v[178:185], v[88:91], v174, v175 op_sel_hi:[0,0,0]
	s_waitcnt lgkmcnt(4)
	v_mfma_scale_f32_16x16x128_f8f6f4 v[76:79], v[0:7], v[186:193], v[76:79], v174, v175 op_sel_hi:[0,0,0]
	v_mfma_scale_f32_16x16x128_f8f6f4 v[72:75], v[8:15], v[186:193], v[72:75], v174, v175 op_sel_hi:[0,0,0]
	s_waitcnt lgkmcnt(2)
	v_mfma_scale_f32_16x16x128_f8f6f4 v[60:63], v[0:7], v[194:201], v[60:63], v174, v175 op_sel_hi:[0,0,0]
	v_mfma_scale_f32_16x16x128_f8f6f4 v[56:59], v[8:15], v[194:201], v[56:59], v174, v175 op_sel_hi:[0,0,0]
	s_waitcnt lgkmcnt(0)
	v_mfma_scale_f32_16x16x128_f8f6f4 v[44:47], v[0:7], v[202:209], v[44:47], v174, v175 op_sel_hi:[0,0,0]
	v_mfma_scale_f32_16x16x128_f8f6f4 v[40:43], v[8:15], v[202:209], v[40:43], v174, v175 op_sel_hi:[0,0,0]
	s_setprio 0
	s_setprio 1
	v_mfma_scale_f32_16x16x128_f8f6f4 v[84:87], v[16:23], v[178:185], v[84:87], v174, v175 op_sel_hi:[0,0,0]
	v_mfma_scale_f32_16x16x128_f8f6f4 v[80:83], v[24:31], v[178:185], v[80:83], v174, v175 op_sel_hi:[0,0,0]
	v_mfma_scale_f32_16x16x128_f8f6f4 v[68:71], v[16:23], v[186:193], v[68:71], v174, v175 op_sel_hi:[0,0,0]
	v_mfma_scale_f32_16x16x128_f8f6f4 v[64:67], v[24:31], v[186:193], v[64:67], v174, v175 op_sel_hi:[0,0,0]
	v_mfma_scale_f32_16x16x128_f8f6f4 v[52:55], v[16:23], v[194:201], v[52:55], v174, v175 op_sel_hi:[0,0,0]
	v_mfma_scale_f32_16x16x128_f8f6f4 v[48:51], v[24:31], v[194:201], v[48:51], v174, v175 op_sel_hi:[0,0,0]
	v_mfma_scale_f32_16x16x128_f8f6f4 v[36:39], v[16:23], v[202:209], v[36:39], v174, v175 op_sel_hi:[0,0,0]
	v_mfma_scale_f32_16x16x128_f8f6f4 v[32:35], v[24:31], v[202:209], v[32:35], v174, v175 op_sel_hi:[0,0,0]
	s_setprio 0
	s_barrier
	s_add_u32 s82, s82, 0x100
	s_addc_u32 s85, s85, 0
	s_add_u32 s86, s86, 0x100
	s_addc_u32 s87, s87, 0
	s_add_u32 s28, s28, 0x100
	s_addc_u32 s29, s29, 0
	s_cmp_ge_i32 s33, s51
	s_mov_b32 s30, s33
	s_cbranch_scc0 .LBB0_544

; #define PG8_STAGE(bufoff, gbase, voff) do { _Pragma("unroll") for (int _i = 0; _i < 2; ++_i) { unsigned keep_; \
;         asm volatile("s_mov_b32 %0, m0\n\ts_mov_b32 m0, %3\n\ts_nop 0\n\tglobal_load_lds_dwordx4 %1, %2\n\ts_mov_b32 m0, %0" : "=&s"(keep_) : "v"((voff)[_i]), "s"((const char*)(gbase)), "s"(ldsb + (unsigned)((bufoff) + _i * 8192)) : "memory"); } } while (0)
; #define PG8_WAIT_V(n) asm volatile("s_waitcnt vmcnt(" #n ")" ::: "memory")
; #define PG8_BAR __builtin_amdgcn_s_barrier()
; template <class Epi, class Sched, bool ALIGN_EPI, bool FP8 = false>
; __device__ __forceinline__ void gemm_phase(PG8_LAS unsigned char* lds, const Gemm g, const Sched& S, const Epi& E, const int wid, const int lane) {
;     ...
;     const int tid = wid * 64 + lane, wr = wid >> 2, wc = wid & 3, fr = lane & 15, fq = lane >> 4;
;     int KB = g.KB; asm volatile("" : "+s"(KB)); const int nt = KB / 128;
;     unsigned voffA[2], voffB[2]; int rA[2]; unsigned cA2[2];
; #pragma unroll
;     for (int i = 0; i < 2; ++i) { int R, C; stage_rc(tid * 16 + i * 8192, R, C); const int Rb = Epi::PERM ? ((R & ~31) + perm32(R & 31)) : R;
;         rA[i] = R; cA2[i] = (unsigned)C * 2u; voffA[i] = (unsigned)(R * KB + C * 2); voffB[i] = (unsigned)(Rb * KB + C * 2); }
;     const size_t kstep = (size_t)(BK * 2);
;     const size_t hstep = (size_t)HALF * KB;
;     const size_t hstepA = GA ? (size_t)0 : hstep;
;     const size_t tstep = 2 * hstep;
;     const unsigned ldsw = (unsigned)wid * 1024u;
;     const int aoff = lds_byte(wr * 64 + fr, fq * 8), boff = lds_byte(wc * 32 + fr, fq * 8);
;     ...
;     const char* cA = GA ? (const char*)g.A : (const char*)g.A + (size_t)cur.pm * tstep; const char* cB = (const char*)g.Bt + (size_t)cur.pn * tstep;
;     PG8_STAGE(PG8_SB(0, 0), cB, voffB); PG8_STAGE(PG8_SB(0, 1), cB + hstep, voffB); PG8_STAGE(PG8_SA(0, 0), cA, vc0); PG8_STAGE(PG8_SA(0, 1), cA + hstepA, vc1);
;     if (wr == 1) PG8_BAR;
;     PG8_WAIT_V(2); PG8_BAR;
;     PG8_STAGE(PG8_SB(1, 0), cB + kstep, voffB); PG8_STAGE(PG8_SA(1, 0), cA + kstep, vc0); PG8_STAGE(PG8_SB(1, 1), cB + hstep + kstep, voffB);
;     PG8_WAIT_V(6); PG8_BAR;
.LBB0_836:
	s_lshr_b32 s5, s5, 25
	s_add_i32 s5, s4, s5
	s_bfe_u32 s26, s90, 0x20006
	v_and_b32_e32 v1, 15, v2
	s_ashr_i32 s52, s5, 7
	v_and_b32_e32 v0, 0xfffffc00, v0
	v_lshl_or_b32 v161, s18, 6, v1
	v_lshl_add_u32 v4, s18, 13, v0
	s_add_u32 s18, s56, 0x4dc00000
	s_addc_u32 s19, s57, 0
	s_add_u32 s20, s56, 0x6f600000
	s_addc_u32 s21, s57, 0
	s_add_u32 s24, s6, 0x80
	s_waitcnt vmcnt(2)
	s_barrier
	s_addc_u32 s25, s7, 0
	s_add_i32 s53, s40, 0x18000
	s_mov_b32 m0, s53
	s_nop 0
	global_load_lds_dwordx4 v162, s[24:25]
	s_add_i32 s54, s40, 0x1a000
	s_mov_b32 m0, s54
	s_nop 0
	global_load_lds_dwordx4 v166, s[24:25]
	s_add_u32 s24, s8, 0x80
	s_addc_u32 s25, s9, 0
	s_add_i32 s55, s40, 0x8000
	s_add_i32 s64, s40, 0xa000
	s_mov_b32 m0, s55
	s_nop 0
	global_load_lds_dwordx4 v160, s[24:25]
	s_add_u32 s22, s22, 0x80
	s_mov_b32 m0, s64
	s_nop 0
	global_load_lds_dwordx4 v164, s[24:25]
	s_addc_u32 s23, s23, 0
	s_add_i32 s65, s40, 0x1c000
	s_add_i32 s66, s40, 0x1e000
	v_and_b32_e32 v3, 48, v2
	s_mov_b32 m0, s65
	s_nop 0
	global_load_lds_dwordx4 v162, s[22:23]
	s_cmpk_gt_i32 s4, 0x7f
	v_lshl_or_b32 v1, v1, 6, v3
	v_lshlrev_b32_e32 v3, 2, v2
	s_mov_b32 m0, s66
	s_nop 0
	global_load_lds_dwordx4 v166, s[22:23]
	s_cselect_b64 s[22:23], -1, 0
	s_add_i32 s67, s52, -2
	s_add_i32 s68, s40, 0xc000
	v_and_b32_e32 v3, 32, v3
	v_lshl_add_u32 v0, s26, 12, v0
	s_cmpk_lt_u32 s90, 0x100
	v_bitop3_b32 v4, v1, v4, v3 bitop3:0xde
	v_bitop3_b32 v0, v1, v0, v3 bitop3:0xde
	s_waitcnt vmcnt(6)
	s_cselect_b64 s[24:25], -1, 0
	v_and_b32_e32 v1, -16, v2
	s_ashr_i32 s4, s76, 3
	v_lshl_add_u32 v163, s26, 6, v1
	s_mul_i32 s70, s4, s3
	v_cndmask_b32_e64 v1, 0, 1, s[0:1]
	v_add_u32_e32 v0, 0, v0
	s_add_i32 s69, s40, 0xe000
	s_add_i32 s70, s70, s27
	v_cmp_ne_u32_e64 s[0:1], 1, v1
	v_add_u32_e32 v165, 0x10000, v0
	v_add_u32_e32 v167, 0x14000, v0
	v_add_u32_e32 v169, 0, v4
	v_mov_b32_e32 v170, 0x79
	v_mov_b32_e32 v171, 0x7b
	v_add_u32_e32 v172, 0x18000, v0
	v_add_u32_e32 v173, 0x1c000, v0
	s_mov_b32 s26, 0x41800000
	s_barrier
	s_mov_b32 s101, 0
	s_branch .LBB0_839

; #define PG8_BAR __builtin_amdgcn_s_barrier()
; template <class Epi, class Sched, bool ALIGN_EPI, bool FP8 = false>
; __device__ __forceinline__ void gemm_phase(PG8_LAS unsigned char* lds, const Gemm g, const Sched& S, const Epi& E, const int wid, const int lane) {
;     ...
;         if (!has_next) break;
; #pragma unroll
;         for (int a = 0; a < 2; ++a)
; #pragma unroll
;             for (int b = 0; b < 2; ++b)
; #pragma unroll
;                 for (int m = 0; m < 4; ++m)
; #pragma unroll
;                     for (int n = 0; n < 2; ++n) acc[a][b][m][n] = (f32x4){0.f, 0.f, 0.f, 0.f};
;         cur = nxt; cA = nA; cB = nB; ++ui;
;         if constexpr (ALIGN_EPI) { if (wr == 1) PG8_BAR; }
.LBB0_838:
	s_mov_b32 s101, 1
	s_andn2_b64 vcc, exec, s[4:5]
	s_mov_b32 s73, s72
	s_mov_b32 s74, s71
	s_mov_b64 s[6:7], s[30:31]
	s_mov_b64 s[8:9], s[28:29]
	s_cbranch_vccz .LBB0_906

; #define PG8_STAGE(bufoff, gbase, voff) do { _Pragma("unroll") for (int _i = 0; _i < 2; ++_i) { unsigned keep_; \
;         asm volatile("s_mov_b32 %0, m0\n\ts_mov_b32 m0, %3\n\ts_nop 0\n\tglobal_load_lds_dwordx4 %1, %2\n\ts_mov_b32 m0, %0" : "=&s"(keep_) : "v"((voff)[_i]), "s"((const char*)(gbase)), "s"(ldsb + (unsigned)((bufoff) + _i * 8192)) : "memory"); } } while (0)
; #define PG8_LDA(dst, b, h) do { _Pragma("unroll") for (int m = 0; m < 4; ++m) _Pragma("unroll") for (int k = 0; k < 2; ++k) dst[m][k] = *(const PG8_LAS bf16x8*)(lds + PG8_SA(b, h) + aoff + m * 2048 + k * 1024); } while (0)
; #define PG8_LDB(dst, b, h) do { _Pragma("unroll") for (int n = 0; n < 2; ++n) _Pragma("unroll") for (int k = 0; k < 2; ++k) dst[n][k] = *(const PG8_LAS bf16x8*)(lds + PG8_SB(b, h) + boff + n * 2048 + k * 1024); } while (0)
; #define PG8_WAIT_V(n) asm volatile("s_waitcnt vmcnt(" #n ")" ::: "memory")
; #define PG8_WAIT_L(n) asm volatile("s_waitcnt lgkmcnt(" #n ")" ::: "memory")
; #define PG8_BAR __builtin_amdgcn_s_barrier()
; #define PG8_SCHED __builtin_amdgcn_sched_barrier(0)
; template <class Epi, class Sched, bool ALIGN_EPI, bool FP8 = false>
; __device__ __forceinline__ void gemm_phase(PG8_LAS unsigned char* lds, const Gemm g, const Sched& S, const Epi& E, const int wid, const int lane) {
;     ...
;             PG8_LDB(B0, 0, 0); PG8_LDB(B1, 0, 1); PG8_SCHED; PG8_LDA(At, 0, 0); PG8_STAGE(PG8_SA(1, 1), a1 + hstepA, vc1);
;             if (GA && last && has_next) { const u32x4 q = *gslot; vc0[0] = q.x; vc0[1] = q.y; vc1[0] = q.z; vc1[1] = q.w; }
;             PG8_WAIT_V(8); PG8_WAIT_L(0); PG8_BAR; PG8_MMA(0, 0, At, B0); PG8_MMA(0, 1, At, B1); PG8_BAR; PG8_SCHED;
.LBB0_852:
	ds_read_b128 v[24:27], v165
	ds_read_b128 v[28:31], v165 offset:1024
	ds_read_b128 v[16:19], v165 offset:2048
	ds_read_b128 v[20:23], v165 offset:3072
	ds_read_b128 v[8:11], v167
	ds_read_b128 v[12:15], v167 offset:1024
	ds_read_b128 v[0:3], v167 offset:2048
	ds_read_b128 v[4:7], v167 offset:3072
	s_add_i32 s33, s8, 2
	s_cmp_eq_u32 s67, s8
	s_cselect_b32 s36, s28, s75
	s_cselect_b32 s37, s29, s82
	s_cselect_b32 s34, s30, s83
	s_cselect_b32 s35, s31, s84
	s_add_u32 s8, s36, 0x80
	s_addc_u32 s9, s37, 0
	ds_read_b128 v[174:177], v169
	ds_read_b128 v[178:181], v169 offset:1024
	ds_read_b128 v[182:185], v169 offset:2048
	ds_read_b128 v[186:189], v169 offset:3072
	ds_read_b128 v[190:193], v169 offset:4096
	ds_read_b128 v[194:197], v169 offset:5120
	ds_read_b128 v[198:201], v169 offset:6144
	ds_read_b128 v[202:205], v169 offset:7168
	s_mov_b32 m0, s68
	s_nop 0
	global_load_lds_dwordx4 v160, s[6:7]
	s_mov_b32 m0, s69
	s_nop 0
	global_load_lds_dwordx4 v164, s[6:7]
	s_cmp_eq_u32 s101, 0
	s_cbranch_scc1 .Lrxn7_0
	s_waitcnt vmcnt(16)
	s_branch .Lrxj7_0

; #define PG8_STAGE(bufoff, gbase, voff) do { _Pragma("unroll") for (int _i = 0; _i < 2; ++_i) { unsigned keep_; \
;         asm volatile("s_mov_b32 %0, m0\n\ts_mov_b32 m0, %3\n\ts_nop 0\n\tglobal_load_lds_dwordx4 %1, %2\n\ts_mov_b32 m0, %0" : "=&s"(keep_) : "v"((voff)[_i]), "s"((const char*)(gbase)), "s"(ldsb + (unsigned)((bufoff) + _i * 8192)) : "memory"); } } while (0)
; #define PG8_LDA(dst, b, h) do { _Pragma("unroll") for (int m = 0; m < 4; ++m) _Pragma("unroll") for (int k = 0; k < 2; ++k) dst[m][k] = *(const PG8_LAS bf16x8*)(lds + PG8_SA(b, h) + aoff + m * 2048 + k * 1024); } while (0)
; #define PG8_WAIT_V(n) asm volatile("s_waitcnt vmcnt(" #n ")" ::: "memory")
; #define PG8_WAIT_L(n) asm volatile("s_waitcnt lgkmcnt(" #n ")" ::: "memory")
; #define PG8_BAR __builtin_amdgcn_s_barrier()
; #define PG8_SCHED __builtin_amdgcn_sched_barrier(0)
; template <class Epi, class Sched, bool ALIGN_EPI, bool FP8 = false>
; __device__ __forceinline__ void gemm_phase(PG8_LAS unsigned char* lds, const Gemm g, const Sched& S, const Epi& E, const int wid, const int lane) {
;     ...
;             PG8_WAIT_V(8); PG8_WAIT_L(0); PG8_BAR; PG8_MMA(0, 0, At, B0); PG8_MMA(0, 1, At, B1); PG8_BAR; PG8_SCHED;
;             PG8_LDA(At, 0, 1); PG8_STAGE(PG8_SB(0, 0), b2, voffB); PG8_STAGE(PG8_SB(0, 1), b2 + hstep, voffB); PG8_STAGE(PG8_SA(0, 0), a2, vc0);
;             PG8_WAIT_V(8); PG8_WAIT_L(0); PG8_BAR; PG8_MMA(1, 0, At, B0); PG8_MMA(1, 1, At, B1); PG8_BAR; PG8_SCHED;
.Lrxj7_0:
	s_waitcnt lgkmcnt(0)
	s_barrier
	s_setprio 1
	s_waitcnt lgkmcnt(6)
	v_mfma_scale_f32_16x16x128_f8f6f4 v[156:159], v[24:31], v[174:181], v[156:159], v170, v171 op_sel_hi:[0,0,0]
	v_mfma_scale_f32_16x16x128_f8f6f4 v[152:155], v[16:23], v[174:181], v[152:155], v170, v171 op_sel_hi:[0,0,0]
	s_waitcnt lgkmcnt(4)
	v_mfma_scale_f32_16x16x128_f8f6f4 v[140:143], v[24:31], v[182:189], v[140:143], v170, v171 op_sel_hi:[0,0,0]
	v_mfma_scale_f32_16x16x128_f8f6f4 v[136:139], v[16:23], v[182:189], v[136:139], v170, v171 op_sel_hi:[0,0,0]
	s_waitcnt lgkmcnt(2)
	v_mfma_scale_f32_16x16x128_f8f6f4 v[124:127], v[24:31], v[190:197], v[124:127], v170, v171 op_sel_hi:[0,0,0]
	v_mfma_scale_f32_16x16x128_f8f6f4 v[120:123], v[16:23], v[190:197], v[120:123], v170, v171 op_sel_hi:[0,0,0]
	s_waitcnt lgkmcnt(0)
	v_mfma_scale_f32_16x16x128_f8f6f4 v[108:111], v[24:31], v[198:205], v[108:111], v170, v171 op_sel_hi:[0,0,0]
	v_mfma_scale_f32_16x16x128_f8f6f4 v[104:107], v[16:23], v[198:205], v[104:107], v170, v171 op_sel_hi:[0,0,0]
	s_setprio 0
	s_setprio 1
	v_mfma_scale_f32_16x16x128_f8f6f4 v[148:151], v[8:15], v[174:181], v[148:151], v170, v171 op_sel_hi:[0,0,0]
	v_mfma_scale_f32_16x16x128_f8f6f4 v[144:147], v[0:7], v[174:181], v[144:147], v170, v171 op_sel_hi:[0,0,0]
	v_mfma_scale_f32_16x16x128_f8f6f4 v[132:135], v[8:15], v[182:189], v[132:135], v170, v171 op_sel_hi:[0,0,0]
	v_mfma_scale_f32_16x16x128_f8f6f4 v[128:131], v[0:7], v[182:189], v[128:131], v170, v171 op_sel_hi:[0,0,0]
	v_mfma_scale_f32_16x16x128_f8f6f4 v[116:119], v[8:15], v[190:197], v[116:119], v170, v171 op_sel_hi:[0,0,0]
	v_mfma_scale_f32_16x16x128_f8f6f4 v[112:115], v[0:7], v[190:197], v[112:115], v170, v171 op_sel_hi:[0,0,0]
	v_mfma_scale_f32_16x16x128_f8f6f4 v[100:103], v[8:15], v[198:205], v[100:103], v170, v171 op_sel_hi:[0,0,0]
	v_mfma_scale_f32_16x16x128_f8f6f4 v[96:99], v[0:7], v[198:205], v[96:99], v170, v171 op_sel_hi:[0,0,0]
	s_setprio 0
	s_barrier
	ds_read_b128 v[174:177], v169 offset:16384
	ds_read_b128 v[178:181], v169 offset:17408
	ds_read_b128 v[182:185], v169 offset:18432
	ds_read_b128 v[186:189], v169 offset:19456
	ds_read_b128 v[190:193], v169 offset:20480
	ds_read_b128 v[194:197], v169 offset:21504
	ds_read_b128 v[198:201], v169 offset:22528
	ds_read_b128 v[202:205], v169 offset:23552
	s_mov_b32 m0, s45
	s_nop 0
	global_load_lds_dwordx4 v162, s[34:35]
	s_mov_b32 m0, s46
	s_nop 0
	global_load_lds_dwordx4 v166, s[34:35]
	s_add_u32 s58, s34, s12
	s_addc_u32 s59, s35, s13
	s_mov_b32 m0, s47
	s_nop 0
	global_load_lds_dwordx4 v162, s[58:59]
	s_mov_b32 m0, s48
	s_nop 0
	global_load_lds_dwordx4 v166, s[58:59]
	s_mov_b32 m0, s40
	s_nop 0
	global_load_lds_dwordx4 v160, s[36:37]
	s_mov_b32 m0, s49
	s_nop 0
	global_load_lds_dwordx4 v164, s[36:37]
	s_cmp_eq_u32 s101, 0
	s_cbranch_scc1 .Lrxn7_1
	s_waitcnt vmcnt(16)
	s_branch .Lrxj7_1

; #define PG8_STAGE(bufoff, gbase, voff) do { _Pragma("unroll") for (int _i = 0; _i < 2; ++_i) { unsigned keep_; \
;         asm volatile("s_mov_b32 %0, m0\n\ts_mov_b32 m0, %3\n\ts_nop 0\n\tglobal_load_lds_dwordx4 %1, %2\n\ts_mov_b32 m0, %0" : "=&s"(keep_) : "v"((voff)[_i]), "s"((const char*)(gbase)), "s"(ldsb + (unsigned)((bufoff) + _i * 8192)) : "memory"); } } while (0)
; #define PG8_LDA(dst, b, h) do { _Pragma("unroll") for (int m = 0; m < 4; ++m) _Pragma("unroll") for (int k = 0; k < 2; ++k) dst[m][k] = *(const PG8_LAS bf16x8*)(lds + PG8_SA(b, h) + aoff + m * 2048 + k * 1024); } while (0)
; #define PG8_LDB(dst, b, h) do { _Pragma("unroll") for (int n = 0; n < 2; ++n) _Pragma("unroll") for (int k = 0; k < 2; ++k) dst[n][k] = *(const PG8_LAS bf16x8*)(lds + PG8_SB(b, h) + boff + n * 2048 + k * 1024); } while (0)
; #define PG8_WAIT_V(n) asm volatile("s_waitcnt vmcnt(" #n ")" ::: "memory")
; #define PG8_WAIT_L(n) asm volatile("s_waitcnt lgkmcnt(" #n ")" ::: "memory")
; #define PG8_BAR __builtin_amdgcn_s_barrier()
; #define PG8_SCHED __builtin_amdgcn_sched_barrier(0)
; template <class Epi, class Sched, bool ALIGN_EPI, bool FP8 = false>
; __device__ __forceinline__ void gemm_phase(PG8_LAS unsigned char* lds, const Gemm g, const Sched& S, const Epi& E, const int wid, const int lane) {
;     ...
;             PG8_WAIT_V(8); PG8_WAIT_L(0); PG8_BAR; PG8_MMA(1, 0, At, B0); PG8_MMA(1, 1, At, B1); PG8_BAR; PG8_SCHED;
;             PG8_LDB(B0, 1, 0); PG8_LDB(B1, 1, 1); PG8_SCHED; PG8_LDA(At, 1, 0); PG8_STAGE(PG8_SA(0, 1), a2 + hstepA, vc1);
;             PG8_WAIT_V(8); PG8_WAIT_L(0); PG8_BAR; PG8_MMA(0, 0, At, B0); PG8_MMA(0, 1, At, B1); PG8_BAR; PG8_SCHED;
.Lrxj7_1:
	s_mov_b32 s101, 0
	s_waitcnt lgkmcnt(0)
	s_barrier
	s_setprio 1
	s_waitcnt lgkmcnt(6)
	v_mfma_scale_f32_16x16x128_f8f6f4 v[92:95], v[24:31], v[174:181], v[92:95], v170, v171 op_sel_hi:[0,0,0]
	v_mfma_scale_f32_16x16x128_f8f6f4 v[88:91], v[16:23], v[174:181], v[88:91], v170, v171 op_sel_hi:[0,0,0]
	s_waitcnt lgkmcnt(4)
	v_mfma_scale_f32_16x16x128_f8f6f4 v[76:79], v[24:31], v[182:189], v[76:79], v170, v171 op_sel_hi:[0,0,0]
	v_mfma_scale_f32_16x16x128_f8f6f4 v[72:75], v[16:23], v[182:189], v[72:75], v170, v171 op_sel_hi:[0,0,0]
	s_waitcnt lgkmcnt(2)
	v_mfma_scale_f32_16x16x128_f8f6f4 v[60:63], v[24:31], v[190:197], v[60:63], v170, v171 op_sel_hi:[0,0,0]
	v_mfma_scale_f32_16x16x128_f8f6f4 v[56:59], v[16:23], v[190:197], v[56:59], v170, v171 op_sel_hi:[0,0,0]
	s_waitcnt lgkmcnt(0)
	v_mfma_scale_f32_16x16x128_f8f6f4 v[44:47], v[24:31], v[198:205], v[44:47], v170, v171 op_sel_hi:[0,0,0]
	v_mfma_scale_f32_16x16x128_f8f6f4 v[40:43], v[16:23], v[198:205], v[40:43], v170, v171 op_sel_hi:[0,0,0]
	s_setprio 0
	s_setprio 1
	v_mfma_scale_f32_16x16x128_f8f6f4 v[84:87], v[8:15], v[174:181], v[84:87], v170, v171 op_sel_hi:[0,0,0]
	v_mfma_scale_f32_16x16x128_f8f6f4 v[80:83], v[0:7], v[174:181], v[80:83], v170, v171 op_sel_hi:[0,0,0]
	v_mfma_scale_f32_16x16x128_f8f6f4 v[68:71], v[8:15], v[182:189], v[68:71], v170, v171 op_sel_hi:[0,0,0]
	v_mfma_scale_f32_16x16x128_f8f6f4 v[64:67], v[0:7], v[182:189], v[64:67], v170, v171 op_sel_hi:[0,0,0]
	v_mfma_scale_f32_16x16x128_f8f6f4 v[52:55], v[8:15], v[190:197], v[52:55], v170, v171 op_sel_hi:[0,0,0]
	v_mfma_scale_f32_16x16x128_f8f6f4 v[48:51], v[0:7], v[190:197], v[48:51], v170, v171 op_sel_hi:[0,0,0]
	v_mfma_scale_f32_16x16x128_f8f6f4 v[36:39], v[8:15], v[198:205], v[36:39], v170, v171 op_sel_hi:[0,0,0]
	v_mfma_scale_f32_16x16x128_f8f6f4 v[32:35], v[0:7], v[198:205], v[32:35], v170, v171 op_sel_hi:[0,0,0]
	s_setprio 0
	s_barrier
	ds_read_b128 v[0:3], v172
	ds_read_b128 v[4:7], v172 offset:1024
	ds_read_b128 v[8:11], v172 offset:2048
	ds_read_b128 v[12:15], v172 offset:3072
	ds_read_b128 v[16:19], v173
	ds_read_b128 v[20:23], v173 offset:1024
	ds_read_b128 v[24:27], v173 offset:2048
	ds_read_b128 v[28:31], v173 offset:3072
	ds_read_b128 v[174:177], v169 offset:32768
	ds_read_b128 v[178:181], v169 offset:33792
	ds_read_b128 v[182:185], v169 offset:34816
	ds_read_b128 v[186:189], v169 offset:35840
	ds_read_b128 v[190:193], v169 offset:36864
	ds_read_b128 v[194:197], v169 offset:37888
	ds_read_b128 v[198:201], v169 offset:38912
	ds_read_b128 v[202:205], v169 offset:39936
	s_add_u32 s36, s36, s12
	s_addc_u32 s37, s37, s13
	s_mov_b32 m0, s50
	s_nop 0
	global_load_lds_dwordx4 v160, s[36:37]
	s_mov_b32 m0, s51
	s_nop 0
	global_load_lds_dwordx4 v164, s[36:37]
	s_waitcnt vmcnt(8)
	s_waitcnt lgkmcnt(0)
	s_barrier
	s_setprio 1
	s_waitcnt lgkmcnt(6)
	v_mfma_scale_f32_16x16x128_f8f6f4 v[156:159], v[0:7], v[174:181], v[156:159], v170, v171 op_sel_hi:[0,0,0]
	v_mfma_scale_f32_16x16x128_f8f6f4 v[152:155], v[8:15], v[174:181], v[152:155], v170, v171 op_sel_hi:[0,0,0]
	s_waitcnt lgkmcnt(4)
	v_mfma_scale_f32_16x16x128_f8f6f4 v[140:143], v[0:7], v[182:189], v[140:143], v170, v171 op_sel_hi:[0,0,0]
	v_mfma_scale_f32_16x16x128_f8f6f4 v[136:139], v[8:15], v[182:189], v[136:139], v170, v171 op_sel_hi:[0,0,0]
	s_waitcnt lgkmcnt(2)
	v_mfma_scale_f32_16x16x128_f8f6f4 v[124:127], v[0:7], v[190:197], v[124:127], v170, v171 op_sel_hi:[0,0,0]
	v_mfma_scale_f32_16x16x128_f8f6f4 v[120:123], v[8:15], v[190:197], v[120:123], v170, v171 op_sel_hi:[0,0,0]
	s_waitcnt lgkmcnt(0)
	v_mfma_scale_f32_16x16x128_f8f6f4 v[108:111], v[0:7], v[198:205], v[108:111], v170, v171 op_sel_hi:[0,0,0]
	v_mfma_scale_f32_16x16x128_f8f6f4 v[104:107], v[8:15], v[198:205], v[104:107], v170, v171 op_sel_hi:[0,0,0]
	s_setprio 0
	s_setprio 1
	v_mfma_scale_f32_16x16x128_f8f6f4 v[148:151], v[16:23], v[174:181], v[148:151], v170, v171 op_sel_hi:[0,0,0]
	v_mfma_scale_f32_16x16x128_f8f6f4 v[144:147], v[24:31], v[174:181], v[144:147], v170, v171 op_sel_hi:[0,0,0]
	v_mfma_scale_f32_16x16x128_f8f6f4 v[132:135], v[16:23], v[182:189], v[132:135], v170, v171 op_sel_hi:[0,0,0]
	v_mfma_scale_f32_16x16x128_f8f6f4 v[128:131], v[24:31], v[182:189], v[128:131], v170, v171 op_sel_hi:[0,0,0]
	v_mfma_scale_f32_16x16x128_f8f6f4 v[116:119], v[16:23], v[190:197], v[116:119], v170, v171 op_sel_hi:[0,0,0]
	v_mfma_scale_f32_16x16x128_f8f6f4 v[112:115], v[24:31], v[190:197], v[112:115], v170, v171 op_sel_hi:[0,0,0]
	v_mfma_scale_f32_16x16x128_f8f6f4 v[100:103], v[16:23], v[198:205], v[100:103], v170, v171 op_sel_hi:[0,0,0]
	v_mfma_scale_f32_16x16x128_f8f6f4 v[96:99], v[24:31], v[198:205], v[96:99], v170, v171 op_sel_hi:[0,0,0]
	s_setprio 0
	s_barrier
; #define PG8_STAGE(bufoff, gbase, voff) do { _Pragma("unroll") for (int _i = 0; _i < 2; ++_i) { unsigned keep_; \
;         asm volatile("s_mov_b32 %0, m0\n\ts_mov_b32 m0, %3\n\ts_nop 0\n\tglobal_load_lds_dwordx4 %1, %2\n\ts_mov_b32 m0, %0" : "=&s"(keep_) : "v"((voff)[_i]), "s"((const char*)(gbase)), "s"(ldsb + (unsigned)((bufoff) + _i * 8192)) : "memory"); } } while (0)
; #define PG8_LDA(dst, b, h) do { _Pragma("unroll") for (int m = 0; m < 4; ++m) _Pragma("unroll") for (int k = 0; k < 2; ++k) dst[m][k] = *(const PG8_LAS bf16x8*)(lds + PG8_SA(b, h) + aoff + m * 2048 + k * 1024); } while (0)
; #define PG8_WAIT_V(n) asm volatile("s_waitcnt vmcnt(" #n ")" ::: "memory")
; #define PG8_WAIT_L(n) asm volatile("s_waitcnt lgkmcnt(" #n ")" ::: "memory")
; #define PG8_BAR __builtin_amdgcn_s_barrier()
; #define PG8_SCHED __builtin_amdgcn_sched_barrier(0)
; template <class Epi, class Sched, bool ALIGN_EPI, bool FP8 = false>
; __device__ __forceinline__ void gemm_phase(PG8_LAS unsigned char* lds, const Gemm g, const Sched& S, const Epi& E, const int wid, const int lane) {
;     ...
;             PG8_LDA(At, 1, 1); PG8_STAGE(PG8_SB(1, 0), b3, voffB); PG8_STAGE(PG8_SB(1, 1), b3 + hstep, voffB); PG8_STAGE(PG8_SA(1, 0), a3, vc0);
;             PG8_WAIT_V(8); PG8_WAIT_L(0); PG8_BAR; PG8_MMA(1, 0, At, B0); PG8_MMA(1, 1, At, B1); PG8_BAR; PG8_SCHED;
	ds_read_b128 v[174:177], v169 offset:49152
	ds_read_b128 v[178:181], v169 offset:50176
	ds_read_b128 v[182:185], v169 offset:51200
	ds_read_b128 v[186:189], v169 offset:52224
	ds_read_b128 v[190:193], v169 offset:53248
	ds_read_b128 v[194:197], v169 offset:54272
	ds_read_b128 v[198:201], v169 offset:55296
	ds_read_b128 v[202:205], v169 offset:56320
	s_add_u32 s34, s34, 0x80
	s_addc_u32 s35, s35, 0
	s_mov_b32 m0, s53
	s_nop 0
	global_load_lds_dwordx4 v162, s[34:35]
	s_mov_b32 m0, s54
	s_nop 0
	global_load_lds_dwordx4 v166, s[34:35]
	s_add_u32 s34, s34, s12
	s_addc_u32 s35, s35, s13
	s_mov_b32 m0, s65
	s_nop 0
	global_load_lds_dwordx4 v162, s[34:35]
	s_mov_b32 m0, s66
	s_nop 0
	global_load_lds_dwordx4 v166, s[34:35]
	s_mov_b32 m0, s55
	s_nop 0
	global_load_lds_dwordx4 v160, s[8:9]
	s_mov_b32 m0, s64
	s_nop 0
	global_load_lds_dwordx4 v164, s[8:9]
	s_waitcnt vmcnt(8)
	s_waitcnt lgkmcnt(0)
	s_barrier
	s_setprio 1
	s_waitcnt lgkmcnt(6)
	v_mfma_scale_f32_16x16x128_f8f6f4 v[92:95], v[0:7], v[174:181], v[92:95], v170, v171 op_sel_hi:[0,0,0]
	v_mfma_scale_f32_16x16x128_f8f6f4 v[88:91], v[8:15], v[174:181], v[88:91], v170, v171 op_sel_hi:[0,0,0]
	s_waitcnt lgkmcnt(4)
	v_mfma_scale_f32_16x16x128_f8f6f4 v[76:79], v[0:7], v[182:189], v[76:79], v170, v171 op_sel_hi:[0,0,0]
	v_mfma_scale_f32_16x16x128_f8f6f4 v[72:75], v[8:15], v[182:189], v[72:75], v170, v171 op_sel_hi:[0,0,0]
	s_waitcnt lgkmcnt(2)
	v_mfma_scale_f32_16x16x128_f8f6f4 v[60:63], v[0:7], v[190:197], v[60:63], v170, v171 op_sel_hi:[0,0,0]
	v_mfma_scale_f32_16x16x128_f8f6f4 v[56:59], v[8:15], v[190:197], v[56:59], v170, v171 op_sel_hi:[0,0,0]
	s_waitcnt lgkmcnt(0)
	v_mfma_scale_f32_16x16x128_f8f6f4 v[44:47], v[0:7], v[198:205], v[44:47], v170, v171 op_sel_hi:[0,0,0]
	v_mfma_scale_f32_16x16x128_f8f6f4 v[40:43], v[8:15], v[198:205], v[40:43], v170, v171 op_sel_hi:[0,0,0]
	s_setprio 0
	s_setprio 1
	v_mfma_scale_f32_16x16x128_f8f6f4 v[84:87], v[16:23], v[174:181], v[84:87], v170, v171 op_sel_hi:[0,0,0]
	v_mfma_scale_f32_16x16x128_f8f6f4 v[80:83], v[24:31], v[174:181], v[80:83], v170, v171 op_sel_hi:[0,0,0]
	v_mfma_scale_f32_16x16x128_f8f6f4 v[68:71], v[16:23], v[182:189], v[68:71], v170, v171 op_sel_hi:[0,0,0]
	v_mfma_scale_f32_16x16x128_f8f6f4 v[64:67], v[24:31], v[182:189], v[64:67], v170, v171 op_sel_hi:[0,0,0]
	v_mfma_scale_f32_16x16x128_f8f6f4 v[52:55], v[16:23], v[190:197], v[52:55], v170, v171 op_sel_hi:[0,0,0]
	v_mfma_scale_f32_16x16x128_f8f6f4 v[48:51], v[24:31], v[190:197], v[48:51], v170, v171 op_sel_hi:[0,0,0]
	v_mfma_scale_f32_16x16x128_f8f6f4 v[36:39], v[16:23], v[198:205], v[36:39], v170, v171 op_sel_hi:[0,0,0]
	v_mfma_scale_f32_16x16x128_f8f6f4 v[32:35], v[24:31], v[198:205], v[32:35], v170, v171 op_sel_hi:[0,0,0]
	s_setprio 0
	s_barrier
	s_add_u32 s75, s75, 0x100
	s_addc_u32 s82, s82, 0
	s_add_u32 s83, s83, 0x100
	s_addc_u32 s84, s84, 0
	s_add_u32 s6, s6, 0x100
	s_addc_u32 s7, s7, 0
	s_cmp_ge_i32 s33, s52
	s_mov_b32 s8, s33
	s_cbranch_scc0 .LBB0_852

; #define PG8_BAR __builtin_amdgcn_s_barrier()
; template <class Epi, class Sched, bool ALIGN_EPI, bool FP8 = false>
; __device__ __forceinline__ void gemm_phase(PG8_LAS unsigned char* lds, const Gemm g, const Sched& S, const Epi& E, const int wid, const int lane) {
;     ...
;         if (!has_next) break;
; #pragma unroll
;         for (int a = 0; a < 2; ++a)
; #pragma unroll
;             for (int b = 0; b < 2; ++b)
; #pragma unroll
;                 for (int m = 0; m < 4; ++m)
; #pragma unroll
;                     for (int n = 0; n < 2; ++n) acc[a][b][m][n] = (f32x4){0.f, 0.f, 0.f, 0.f};
;         cur = nxt; cA = nA; cB = nB; ++ui;
;         if constexpr (ALIGN_EPI) { if (wr == 1) PG8_BAR; }
;     }
.LBB0_1125:
	s_mov_b32 s101, 1
	s_andn2_b64 vcc, exec, s[0:1]
	s_mov_b32 s83, s74
	s_mov_b32 s84, s75
	s_mov_b64 s[26:27], s[24:25]
	s_mov_b64 s[28:29], s[22:23]
	s_cbranch_vccz .LBB0_1208

; #define PG8_STAGE(bufoff, gbase, voff) do { _Pragma("unroll") for (int _i = 0; _i < 2; ++_i) { unsigned keep_; \
;         asm volatile("s_mov_b32 %0, m0\n\ts_mov_b32 m0, %3\n\ts_nop 0\n\tglobal_load_lds_dwordx4 %1, %2\n\ts_mov_b32 m0, %0" : "=&s"(keep_) : "v"((voff)[_i]), "s"((const char*)(gbase)), "s"(ldsb + (unsigned)((bufoff) + _i * 8192)) : "memory"); } } while (0)
; #define PG8_WAIT_V(n) asm volatile("s_waitcnt vmcnt(" #n ")" ::: "memory")
; #define PG8_BAR __builtin_amdgcn_s_barrier()
; template <class Epi, class Sched, bool ALIGN_EPI, bool FP8 = false>
; __device__ __forceinline__ void gemm_phase(PG8_LAS unsigned char* lds, const Gemm g, const Sched& S, const Epi& E, const int wid, const int lane) {
;     ...
;     const int tid = wid * 64 + lane, wr = wid >> 2, wc = wid & 3, fr = lane & 15, fq = lane >> 4;
;     int KB = g.KB; asm volatile("" : "+s"(KB)); const int nt = KB / 128;
;     unsigned voffA[2], voffB[2]; int rA[2]; unsigned cA2[2];
; #pragma unroll
;     for (int i = 0; i < 2; ++i) { int R, C; stage_rc(tid * 16 + i * 8192, R, C); const int Rb = Epi::PERM ? ((R & ~31) + perm32(R & 31)) : R;
;         rA[i] = R; cA2[i] = (unsigned)C * 2u; voffA[i] = (unsigned)(R * KB + C * 2); voffB[i] = (unsigned)(Rb * KB + C * 2); }
;     const size_t kstep = (size_t)(BK * 2);
;     const size_t hstep = (size_t)HALF * KB;
;     const size_t hstepA = GA ? (size_t)0 : hstep;
;     const size_t tstep = 2 * hstep;
;     const unsigned ldsw = (unsigned)wid * 1024u;
;     const int aoff = lds_byte(wr * 64 + fr, fq * 8), boff = lds_byte(wc * 32 + fr, fq * 8);
;     ...
;     if (wr == 1) PG8_BAR;
;     PG8_WAIT_V(2); PG8_BAR;
;     PG8_STAGE(PG8_SB(1, 0), cB + kstep, voffB); PG8_STAGE(PG8_SA(1, 0), cA + kstep, vc0); PG8_STAGE(PG8_SB(1, 1), cB + hstep + kstep, voffB);
;     PG8_WAIT_V(6); PG8_BAR;
;     for (;;) {
.LBB0_1439:
	s_sext_i32_i8 s83, s12
	s_add_u32 s12, s56, 0x55c00000
	s_addc_u32 s13, s57, 0
	s_lshr_b32 s1, s1, 25
	s_add_i32 s1, s0, s1
	s_ashr_i32 s51, s1, 7
	v_ashrrev_i32_e32 v2, 6, v172
	s_lshl_b32 s1, s14, 13
	v_lshl_add_u32 v4, v2, 10, s1
	s_lshl_b32 s1, s80, 5
	v_and_b32_e32 v0, 15, v172
	s_and_b32 s1, s1, 0x60
	v_lshl_or_b32 v161, s14, 6, v0
	s_lshr_b32 s14, s1, 3
	v_add_lshl_u32 v2, v2, s14, 10
	s_add_u32 s14, s28, 0x80
	s_waitcnt vmcnt(2)
	s_barrier
	s_addc_u32 s15, s29, 0
	s_add_i32 s52, s42, 0x18000
	s_mov_b32 m0, s52
	s_nop 0
	global_load_lds_dwordx4 v162, s[14:15]
	s_add_i32 s53, s42, 0x1a000
	s_mov_b32 m0, s53
	s_nop 0
	global_load_lds_dwordx4 v166, s[14:15]
	s_add_u32 s14, s30, 0x80
	s_addc_u32 s15, s31, 0
	s_add_i32 s54, s42, 0x8000
	s_mov_b32 m0, s54
	s_nop 0
	global_load_lds_dwordx4 v160, s[14:15]
	s_add_i32 s55, s42, 0xa000
	v_and_b32_e32 v3, 48, v172
	s_mov_b32 m0, s55
	s_nop 0
	global_load_lds_dwordx4 v164, s[14:15]
	s_add_u32 s4, s4, 0x80
	v_lshl_or_b32 v0, v0, 6, v3
	v_lshlrev_b32_e32 v3, 2, v172
	s_addc_u32 s5, s5, 0
	s_add_i32 s64, s42, 0x1c000
	s_mov_b32 m0, s64
	s_nop 0
	global_load_lds_dwordx4 v162, s[4:5]
	s_add_i32 s65, s42, 0x1e000
	v_and_b32_e32 v3, 32, v3
	s_mov_b32 m0, s65
	s_nop 0
	global_load_lds_dwordx4 v166, s[4:5]
	s_cmpk_gt_i32 s0, 0x7f
	v_ashrrev_i32_e32 v1, 1, v172
	v_bitop3_b32 v4, v0, v4, v3 bitop3:0xde
	v_bitop3_b32 v0, v0, v2, v3 bitop3:0xde
	s_waitcnt vmcnt(6)
	s_cselect_b64 s[14:15], -1, 0
	s_add_i32 s66, s51, -2
	s_add_i32 s67, s42, 0xc000
	v_and_b32_e32 v1, -8, v1
	s_cmpk_lt_u32 s90, 0x100
	v_add_u32_e32 v0, 0, v0
	s_cselect_b64 s[16:17], -1, 0
	v_add_u32_e32 v163, s1, v1
	s_add_i32 s68, s42, 0xe000
	s_ashr_i32 s69, s76, 31
	v_mov_b64_e32 v[168:169], 0x200
	v_mov_b64_e32 v[170:171], 0x1ff
	v_add_u32_e32 v165, 0x10000, v0
	v_add_u32_e32 v167, 0x14000, v0
	v_add_u32_e32 v173, 0, v4
	v_mov_b32_e32 v174, 0x79
	v_mov_b32_e32 v175, 0x7b
	v_add_u32_e32 v176, 0x18000, v0
	v_add_u32_e32 v177, 0x1c000, v0
	s_mov_b64 s[18:19], 0x80000
	s_mov_b32 s70, 0x80000
	s_mov_b64 s[20:21], 0x90000
	s_mov_b32 s71, 0x90000
	s_mov_b64 s[22:23], 0xa0000
	s_mov_b32 s72, 0xa0000
	s_mov_b64 s[24:25], 0xb0000
	s_mov_b32 s73, 0xb0000
	s_barrier
	s_waitcnt vmcnt(0)
	s_mov_b32 s101, 0
	s_branch .LBB0_1442

; #define PG8_BAR __builtin_amdgcn_s_barrier()
; template <class Epi, class Sched, bool ALIGN_EPI, bool FP8 = false>
; __device__ __forceinline__ void gemm_phase(PG8_LAS unsigned char* lds, const Gemm g, const Sched& S, const Epi& E, const int wid, const int lane) {
;     ...
;         if (!has_next) break;
; #pragma unroll
;         for (int a = 0; a < 2; ++a)
; #pragma unroll
;             for (int b = 0; b < 2; ++b)
; #pragma unroll
;                 for (int m = 0; m < 4; ++m)
; #pragma unroll
;                     for (int n = 0; n < 2; ++n) acc[a][b][m][n] = (f32x4){0.f, 0.f, 0.f, 0.f};
;         cur = nxt; cA = nA; cB = nB; ++ui;
;         if constexpr (ALIGN_EPI) { if (wr == 1) PG8_BAR; }
;     }
.LBB0_1441:
	s_mov_b32 s101, 1
	s_andn2_b64 vcc, exec, s[0:1]
	s_mov_b32 s83, s74
	s_mov_b32 s82, s75
	s_mov_b64 s[28:29], s[26:27]
	s_mov_b64 s[30:31], s[4:5]
	s_cbranch_vccz .LBB0_1460

; #define PG8_STAGE(bufoff, gbase, voff) do { _Pragma("unroll") for (int _i = 0; _i < 2; ++_i) { unsigned keep_; \
;         asm volatile("s_mov_b32 %0, m0\n\ts_mov_b32 m0, %3\n\ts_nop 0\n\tglobal_load_lds_dwordx4 %1, %2\n\ts_mov_b32 m0, %0" : "=&s"(keep_) : "v"((voff)[_i]), "s"((const char*)(gbase)), "s"(ldsb + (unsigned)((bufoff) + _i * 8192)) : "memory"); } } while (0)
; #define PG8_LDA(dst, b, h) do { _Pragma("unroll") for (int m = 0; m < 4; ++m) _Pragma("unroll") for (int k = 0; k < 2; ++k) dst[m][k] = *(const PG8_LAS bf16x8*)(lds + PG8_SA(b, h) + aoff + m * 2048 + k * 1024); } while (0)
; #define PG8_LDB(dst, b, h) do { _Pragma("unroll") for (int n = 0; n < 2; ++n) _Pragma("unroll") for (int k = 0; k < 2; ++k) dst[n][k] = *(const PG8_LAS bf16x8*)(lds + PG8_SB(b, h) + boff + n * 2048 + k * 1024); } while (0)
; #define PG8_WAIT_V(n) asm volatile("s_waitcnt vmcnt(" #n ")" ::: "memory")
; #define PG8_WAIT_L(n) asm volatile("s_waitcnt lgkmcnt(" #n ")" ::: "memory")
; #define PG8_BAR __builtin_amdgcn_s_barrier()
; #define PG8_SCHED __builtin_amdgcn_sched_barrier(0)
; template <class Epi, class Sched, bool ALIGN_EPI, bool FP8 = false>
; __device__ __forceinline__ void gemm_phase(PG8_LAS unsigned char* lds, const Gemm g, const Sched& S, const Epi& E, const int wid, const int lane) {
;     ...
;         for (int t = 0; t < nt; t += 2) {
;             const bool last = (t == nt - 2);
;             const char* a1 = cA + (size_t)(t + 1) * kstep;
;             const char* a2 = last ? nA : cA + (size_t)(t + 2) * kstep; const char* b2 = last ? nB : cB + (size_t)(t + 2) * kstep;
;             const char* a3 = a2 + kstep; const char* b3 = b2 + kstep;
;             PG8_LDB(B0, 0, 0); PG8_LDB(B1, 0, 1); PG8_SCHED; PG8_LDA(At, 0, 0); PG8_STAGE(PG8_SA(1, 1), a1 + hstepA, vc1);
;             if (GA && last && has_next) { const u32x4 q = *gslot; vc0[0] = q.x; vc0[1] = q.y; vc1[0] = q.z; vc1[1] = q.w; }
;             PG8_WAIT_V(8); PG8_WAIT_L(0); PG8_BAR; PG8_MMA(0, 0, At, B0); PG8_MMA(0, 1, At, B1); PG8_BAR; PG8_SCHED;
.LBB0_1454:
	ds_read_b128 v[24:27], v165
	ds_read_b128 v[28:31], v165 offset:1024
	ds_read_b128 v[16:19], v165 offset:2048
	ds_read_b128 v[20:23], v165 offset:3072
	ds_read_b128 v[8:11], v167
	ds_read_b128 v[12:15], v167 offset:1024
	ds_read_b128 v[0:3], v167 offset:2048
	ds_read_b128 v[4:7], v167 offset:3072
	s_add_i32 s33, s30, 2
	s_cmp_eq_u32 s66, s30
	s_cselect_b32 s36, s4, s84
	s_cselect_b32 s37, s5, s85
	s_cselect_b32 s34, s26, s86
	s_cselect_b32 s35, s27, s87
	s_add_u32 s30, s36, 0x80
	s_addc_u32 s31, s37, 0
	ds_read_b128 v[178:181], v173
	ds_read_b128 v[182:185], v173 offset:1024
	ds_read_b128 v[186:189], v173 offset:2048
	ds_read_b128 v[190:193], v173 offset:3072
	ds_read_b128 v[194:197], v173 offset:4096
	ds_read_b128 v[198:201], v173 offset:5120
	ds_read_b128 v[202:205], v173 offset:6144
	ds_read_b128 v[206:209], v173 offset:7168
	s_mov_b32 m0, s67
	s_nop 0
	global_load_lds_dwordx4 v160, s[28:29]
	s_mov_b32 m0, s68
	s_nop 0
	global_load_lds_dwordx4 v164, s[28:29]
	s_cmp_eq_u32 s101, 0
	s_cbranch_scc1 .Lrxn12_0
	s_waitcnt vmcnt(24)
	s_branch .Lrxj12_0

; #define PG8_STAGE(bufoff, gbase, voff) do { _Pragma("unroll") for (int _i = 0; _i < 2; ++_i) { unsigned keep_; \
;         asm volatile("s_mov_b32 %0, m0\n\ts_mov_b32 m0, %3\n\ts_nop 0\n\tglobal_load_lds_dwordx4 %1, %2\n\ts_mov_b32 m0, %0" : "=&s"(keep_) : "v"((voff)[_i]), "s"((const char*)(gbase)), "s"(ldsb + (unsigned)((bufoff) + _i * 8192)) : "memory"); } } while (0)
; #define PG8_LDA(dst, b, h) do { _Pragma("unroll") for (int m = 0; m < 4; ++m) _Pragma("unroll") for (int k = 0; k < 2; ++k) dst[m][k] = *(const PG8_LAS bf16x8*)(lds + PG8_SA(b, h) + aoff + m * 2048 + k * 1024); } while (0)
; #define PG8_LDB(dst, b, h) do { _Pragma("unroll") for (int n = 0; n < 2; ++n) _Pragma("unroll") for (int k = 0; k < 2; ++k) dst[n][k] = *(const PG8_LAS bf16x8*)(lds + PG8_SB(b, h) + boff + n * 2048 + k * 1024); } while (0)
; #define PG8_WAIT_V(n) asm volatile("s_waitcnt vmcnt(" #n ")" ::: "memory")
; #define PG8_WAIT_L(n) asm volatile("s_waitcnt lgkmcnt(" #n ")" ::: "memory")
; #define PG8_BAR __builtin_amdgcn_s_barrier()
; #define PG8_SCHED __builtin_amdgcn_sched_barrier(0)
; template <class Epi, class Sched, bool ALIGN_EPI, bool FP8 = false>
; __device__ __forceinline__ void gemm_phase(PG8_LAS unsigned char* lds, const Gemm g, const Sched& S, const Epi& E, const int wid, const int lane) {
;     ...
;             PG8_WAIT_V(8); PG8_WAIT_L(0); PG8_BAR; PG8_MMA(1, 0, At, B0); PG8_MMA(1, 1, At, B1); PG8_BAR; PG8_SCHED;
;             PG8_LDB(B0, 1, 0); PG8_LDB(B1, 1, 1); PG8_SCHED; PG8_LDA(At, 1, 0); PG8_STAGE(PG8_SA(0, 1), a2 + hstepA, vc1);
;             PG8_WAIT_V(8); PG8_WAIT_L(0); PG8_BAR; PG8_MMA(0, 0, At, B0); PG8_MMA(0, 1, At, B1); PG8_BAR; PG8_SCHED;
.Lrxj12_1:
	s_mov_b32 s101, 0
	s_waitcnt lgkmcnt(0)
	s_barrier
	s_setprio 1
	s_waitcnt lgkmcnt(6)
	v_mfma_scale_f32_16x16x128_f8f6f4 v[92:95], v[24:31], v[178:185], v[92:95], v174, v175 op_sel_hi:[0,0,0]
	v_mfma_scale_f32_16x16x128_f8f6f4 v[88:91], v[16:23], v[178:185], v[88:91], v174, v175 op_sel_hi:[0,0,0]
	s_waitcnt lgkmcnt(4)
	v_mfma_scale_f32_16x16x128_f8f6f4 v[76:79], v[24:31], v[186:193], v[76:79], v174, v175 op_sel_hi:[0,0,0]
	v_mfma_scale_f32_16x16x128_f8f6f4 v[72:75], v[16:23], v[186:193], v[72:75], v174, v175 op_sel_hi:[0,0,0]
	s_waitcnt lgkmcnt(2)
	v_mfma_scale_f32_16x16x128_f8f6f4 v[60:63], v[24:31], v[194:201], v[60:63], v174, v175 op_sel_hi:[0,0,0]
	v_mfma_scale_f32_16x16x128_f8f6f4 v[56:59], v[16:23], v[194:201], v[56:59], v174, v175 op_sel_hi:[0,0,0]
	s_waitcnt lgkmcnt(0)
	v_mfma_scale_f32_16x16x128_f8f6f4 v[44:47], v[24:31], v[202:209], v[44:47], v174, v175 op_sel_hi:[0,0,0]
	v_mfma_scale_f32_16x16x128_f8f6f4 v[40:43], v[16:23], v[202:209], v[40:43], v174, v175 op_sel_hi:[0,0,0]
	s_setprio 0
	s_setprio 1
	v_mfma_scale_f32_16x16x128_f8f6f4 v[84:87], v[8:15], v[178:185], v[84:87], v174, v175 op_sel_hi:[0,0,0]
	v_mfma_scale_f32_16x16x128_f8f6f4 v[80:83], v[0:7], v[178:185], v[80:83], v174, v175 op_sel_hi:[0,0,0]
	v_mfma_scale_f32_16x16x128_f8f6f4 v[68:71], v[8:15], v[186:193], v[68:71], v174, v175 op_sel_hi:[0,0,0]
	v_mfma_scale_f32_16x16x128_f8f6f4 v[64:67], v[0:7], v[186:193], v[64:67], v174, v175 op_sel_hi:[0,0,0]
	v_mfma_scale_f32_16x16x128_f8f6f4 v[52:55], v[8:15], v[194:201], v[52:55], v174, v175 op_sel_hi:[0,0,0]
	v_mfma_scale_f32_16x16x128_f8f6f4 v[48:51], v[0:7], v[194:201], v[48:51], v174, v175 op_sel_hi:[0,0,0]
	v_mfma_scale_f32_16x16x128_f8f6f4 v[36:39], v[8:15], v[202:209], v[36:39], v174, v175 op_sel_hi:[0,0,0]
	v_mfma_scale_f32_16x16x128_f8f6f4 v[32:35], v[0:7], v[202:209], v[32:35], v174, v175 op_sel_hi:[0,0,0]
	s_setprio 0
	s_barrier
	ds_read_b128 v[0:3], v176
	ds_read_b128 v[4:7], v176 offset:1024
	ds_read_b128 v[8:11], v176 offset:2048
	ds_read_b128 v[12:15], v176 offset:3072
	ds_read_b128 v[16:19], v177
	ds_read_b128 v[20:23], v177 offset:1024
	ds_read_b128 v[24:27], v177 offset:2048
	ds_read_b128 v[28:31], v177 offset:3072
	ds_read_b128 v[178:181], v173 offset:32768
	ds_read_b128 v[182:185], v173 offset:33792
	ds_read_b128 v[186:189], v173 offset:34816
	ds_read_b128 v[190:193], v173 offset:35840
	ds_read_b128 v[194:197], v173 offset:36864
	ds_read_b128 v[198:201], v173 offset:37888
	ds_read_b128 v[202:205], v173 offset:38912
	ds_read_b128 v[206:209], v173 offset:39936
	s_add_u32 s36, s36, s6
	s_addc_u32 s37, s37, s7
	s_mov_b32 m0, s49
	s_nop 0
	global_load_lds_dwordx4 v160, s[36:37]
	s_mov_b32 m0, s50
	s_nop 0
	global_load_lds_dwordx4 v164, s[36:37]
	s_waitcnt vmcnt(8)
	s_waitcnt lgkmcnt(0)
	s_barrier
	s_setprio 1
	s_waitcnt lgkmcnt(6)
	v_mfma_scale_f32_16x16x128_f8f6f4 v[156:159], v[0:7], v[178:185], v[156:159], v174, v175 op_sel_hi:[0,0,0]
	v_mfma_scale_f32_16x16x128_f8f6f4 v[152:155], v[8:15], v[178:185], v[152:155], v174, v175 op_sel_hi:[0,0,0]
	s_waitcnt lgkmcnt(4)
	v_mfma_scale_f32_16x16x128_f8f6f4 v[140:143], v[0:7], v[186:193], v[140:143], v174, v175 op_sel_hi:[0,0,0]
	v_mfma_scale_f32_16x16x128_f8f6f4 v[136:139], v[8:15], v[186:193], v[136:139], v174, v175 op_sel_hi:[0,0,0]
	s_waitcnt lgkmcnt(2)
	v_mfma_scale_f32_16x16x128_f8f6f4 v[124:127], v[0:7], v[194:201], v[124:127], v174, v175 op_sel_hi:[0,0,0]
	v_mfma_scale_f32_16x16x128_f8f6f4 v[120:123], v[8:15], v[194:201], v[120:123], v174, v175 op_sel_hi:[0,0,0]
	s_waitcnt lgkmcnt(0)
	v_mfma_scale_f32_16x16x128_f8f6f4 v[108:111], v[0:7], v[202:209], v[108:111], v174, v175 op_sel_hi:[0,0,0]
	v_mfma_scale_f32_16x16x128_f8f6f4 v[104:107], v[8:15], v[202:209], v[104:107], v174, v175 op_sel_hi:[0,0,0]
	s_setprio 0
	s_setprio 1
	v_mfma_scale_f32_16x16x128_f8f6f4 v[148:151], v[16:23], v[178:185], v[148:151], v174, v175 op_sel_hi:[0,0,0]
	v_mfma_scale_f32_16x16x128_f8f6f4 v[144:147], v[24:31], v[178:185], v[144:147], v174, v175 op_sel_hi:[0,0,0]
	v_mfma_scale_f32_16x16x128_f8f6f4 v[132:135], v[16:23], v[186:193], v[132:135], v174, v175 op_sel_hi:[0,0,0]
	v_mfma_scale_f32_16x16x128_f8f6f4 v[128:131], v[24:31], v[186:193], v[128:131], v174, v175 op_sel_hi:[0,0,0]
	v_mfma_scale_f32_16x16x128_f8f6f4 v[116:119], v[16:23], v[194:201], v[116:119], v174, v175 op_sel_hi:[0,0,0]
	v_mfma_scale_f32_16x16x128_f8f6f4 v[112:115], v[24:31], v[194:201], v[112:115], v174, v175 op_sel_hi:[0,0,0]
	v_mfma_scale_f32_16x16x128_f8f6f4 v[100:103], v[16:23], v[202:209], v[100:103], v174, v175 op_sel_hi:[0,0,0]
	v_mfma_scale_f32_16x16x128_f8f6f4 v[96:99], v[24:31], v[202:209], v[96:99], v174, v175 op_sel_hi:[0,0,0]
	s_setprio 0
	s_barrier
; #define PG8_STAGE(bufoff, gbase, voff) do { _Pragma("unroll") for (int _i = 0; _i < 2; ++_i) { unsigned keep_; \
;         asm volatile("s_mov_b32 %0, m0\n\ts_mov_b32 m0, %3\n\ts_nop 0\n\tglobal_load_lds_dwordx4 %1, %2\n\ts_mov_b32 m0, %0" : "=&s"(keep_) : "v"((voff)[_i]), "s"((const char*)(gbase)), "s"(ldsb + (unsigned)((bufoff) + _i * 8192)) : "memory"); } } while (0)
; #define PG8_LDA(dst, b, h) do { _Pragma("unroll") for (int m = 0; m < 4; ++m) _Pragma("unroll") for (int k = 0; k < 2; ++k) dst[m][k] = *(const PG8_LAS bf16x8*)(lds + PG8_SA(b, h) + aoff + m * 2048 + k * 1024); } while (0)
; #define PG8_WAIT_V(n) asm volatile("s_waitcnt vmcnt(" #n ")" ::: "memory")
; #define PG8_WAIT_L(n) asm volatile("s_waitcnt lgkmcnt(" #n ")" ::: "memory")
; #define PG8_BAR __builtin_amdgcn_s_barrier()
; #define PG8_SCHED __builtin_amdgcn_sched_barrier(0)
; template <class Epi, class Sched, bool ALIGN_EPI, bool FP8 = false>
; __device__ __forceinline__ void gemm_phase(PG8_LAS unsigned char* lds, const Gemm g, const Sched& S, const Epi& E, const int wid, const int lane) {
;     ...
;             PG8_LDA(At, 1, 1); PG8_STAGE(PG8_SB(1, 0), b3, voffB); PG8_STAGE(PG8_SB(1, 1), b3 + hstep, voffB); PG8_STAGE(PG8_SA(1, 0), a3, vc0);
;             PG8_WAIT_V(8); PG8_WAIT_L(0); PG8_BAR; PG8_MMA(1, 0, At, B0); PG8_MMA(1, 1, At, B1); PG8_BAR; PG8_SCHED;
	ds_read_b128 v[178:181], v173 offset:49152
	ds_read_b128 v[182:185], v173 offset:50176
	ds_read_b128 v[186:189], v173 offset:51200
	ds_read_b128 v[190:193], v173 offset:52224
	ds_read_b128 v[194:197], v173 offset:53248
	ds_read_b128 v[198:201], v173 offset:54272
	ds_read_b128 v[202:205], v173 offset:55296
	ds_read_b128 v[206:209], v173 offset:56320
	s_add_u32 s34, s34, 0x80
	s_addc_u32 s35, s35, 0
	s_mov_b32 m0, s52
	s_nop 0
	global_load_lds_dwordx4 v162, s[34:35]
	s_mov_b32 m0, s53
	s_nop 0
	global_load_lds_dwordx4 v166, s[34:35]
	s_add_u32 s34, s34, s6
	s_addc_u32 s35, s35, s7
	s_mov_b32 m0, s64
	s_nop 0
	global_load_lds_dwordx4 v162, s[34:35]
	s_mov_b32 m0, s65
	s_nop 0
	global_load_lds_dwordx4 v166, s[34:35]
	s_mov_b32 m0, s54
	s_nop 0
	global_load_lds_dwordx4 v160, s[30:31]
	s_mov_b32 m0, s55
	s_nop 0
	global_load_lds_dwordx4 v164, s[30:31]
	s_waitcnt vmcnt(8)
	s_waitcnt lgkmcnt(0)
	s_barrier
	s_setprio 1
	s_waitcnt lgkmcnt(6)
	v_mfma_scale_f32_16x16x128_f8f6f4 v[92:95], v[0:7], v[178:185], v[92:95], v174, v175 op_sel_hi:[0,0,0]
	v_mfma_scale_f32_16x16x128_f8f6f4 v[88:91], v[8:15], v[178:185], v[88:91], v174, v175 op_sel_hi:[0,0,0]
	s_waitcnt lgkmcnt(4)
	v_mfma_scale_f32_16x16x128_f8f6f4 v[76:79], v[0:7], v[186:193], v[76:79], v174, v175 op_sel_hi:[0,0,0]
	v_mfma_scale_f32_16x16x128_f8f6f4 v[72:75], v[8:15], v[186:193], v[72:75], v174, v175 op_sel_hi:[0,0,0]
	s_waitcnt lgkmcnt(2)
	v_mfma_scale_f32_16x16x128_f8f6f4 v[60:63], v[0:7], v[194:201], v[60:63], v174, v175 op_sel_hi:[0,0,0]
	v_mfma_scale_f32_16x16x128_f8f6f4 v[56:59], v[8:15], v[194:201], v[56:59], v174, v175 op_sel_hi:[0,0,0]
	s_waitcnt lgkmcnt(0)
	v_mfma_scale_f32_16x16x128_f8f6f4 v[44:47], v[0:7], v[202:209], v[44:47], v174, v175 op_sel_hi:[0,0,0]
	v_mfma_scale_f32_16x16x128_f8f6f4 v[40:43], v[8:15], v[202:209], v[40:43], v174, v175 op_sel_hi:[0,0,0]
	s_setprio 0
	s_setprio 1
	v_mfma_scale_f32_16x16x128_f8f6f4 v[84:87], v[16:23], v[178:185], v[84:87], v174, v175 op_sel_hi:[0,0,0]
	v_mfma_scale_f32_16x16x128_f8f6f4 v[80:83], v[24:31], v[178:185], v[80:83], v174, v175 op_sel_hi:[0,0,0]
	v_mfma_scale_f32_16x16x128_f8f6f4 v[68:71], v[16:23], v[186:193], v[68:71], v174, v175 op_sel_hi:[0,0,0]
	v_mfma_scale_f32_16x16x128_f8f6f4 v[64:67], v[24:31], v[186:193], v[64:67], v174, v175 op_sel_hi:[0,0,0]
	v_mfma_scale_f32_16x16x128_f8f6f4 v[52:55], v[16:23], v[194:201], v[52:55], v174, v175 op_sel_hi:[0,0,0]
	v_mfma_scale_f32_16x16x128_f8f6f4 v[48:51], v[24:31], v[194:201], v[48:51], v174, v175 op_sel_hi:[0,0,0]
	v_mfma_scale_f32_16x16x128_f8f6f4 v[36:39], v[16:23], v[202:209], v[36:39], v174, v175 op_sel_hi:[0,0,0]
	v_mfma_scale_f32_16x16x128_f8f6f4 v[32:35], v[24:31], v[202:209], v[32:35], v174, v175 op_sel_hi:[0,0,0]
	s_setprio 0
	s_barrier
	s_add_u32 s84, s84, 0x100
	s_addc_u32 s85, s85, 0
	s_add_u32 s86, s86, 0x100
	s_addc_u32 s87, s87, 0
	s_add_u32 s28, s28, 0x100
	s_addc_u32 s29, s29, 0
	s_cmp_ge_i32 s33, s51
	s_mov_b32 s30, s33
	s_cbranch_scc0 .LBB0_1454

; #define PG8_STAGE(bufoff, gbase, voff) do { _Pragma("unroll") for (int _i = 0; _i < 2; ++_i) { unsigned keep_; \
;         asm volatile("s_mov_b32 %0, m0\n\ts_mov_b32 m0, %3\n\ts_nop 0\n\tglobal_load_lds_dwordx4 %1, %2\n\ts_mov_b32 m0, %0" : "=&s"(keep_) : "v"((voff)[_i]), "s"((const char*)(gbase)), "s"(ldsb + (unsigned)((bufoff) + _i * 8192)) : "memory"); } } while (0)
; #define PG8_LDA(dst, b, h) do { _Pragma("unroll") for (int m = 0; m < 4; ++m) _Pragma("unroll") for (int k = 0; k < 2; ++k) dst[m][k] = *(const PG8_LAS bf16x8*)(lds + PG8_SA(b, h) + aoff + m * 2048 + k * 1024); } while (0)
; #define PG8_LDB(dst, b, h) do { _Pragma("unroll") for (int n = 0; n < 2; ++n) _Pragma("unroll") for (int k = 0; k < 2; ++k) dst[n][k] = *(const PG8_LAS bf16x8*)(lds + PG8_SB(b, h) + boff + n * 2048 + k * 1024); } while (0)
; #define PG8_WAIT_V(n) asm volatile("s_waitcnt vmcnt(" #n ")" ::: "memory")
; #define PG8_WAIT_L(n) asm volatile("s_waitcnt lgkmcnt(" #n ")" ::: "memory")
; #define PG8_BAR __builtin_amdgcn_s_barrier()
; #define PG8_SCHED __builtin_amdgcn_sched_barrier(0)
; template <class Epi, class Sched, bool ALIGN_EPI, bool FP8 = false>
; __device__ __forceinline__ void gemm_phase(PG8_LAS unsigned char* lds, const Gemm g, const Sched& S, const Epi& E, const int wid, const int lane) {
;     ...
;         for (int t = 0; t < nt; t += 2) {
;             const bool last = (t == nt - 2);
;             const char* a1 = cA + (size_t)(t + 1) * kstep;
;             const char* a2 = last ? nA : cA + (size_t)(t + 2) * kstep; const char* b2 = last ? nB : cB + (size_t)(t + 2) * kstep;
;             const char* a3 = a2 + kstep; const char* b3 = b2 + kstep;
;             PG8_LDB(B0, 0, 0); PG8_LDB(B1, 0, 1); PG8_SCHED; PG8_LDA(At, 0, 0); PG8_STAGE(PG8_SA(1, 1), a1 + hstepA, vc1);
;             if (GA && last && has_next) { const u32x4 q = *gslot; vc0[0] = q.x; vc0[1] = q.y; vc1[0] = q.z; vc1[1] = q.w; }
;             PG8_WAIT_V(8); PG8_WAIT_L(0); PG8_BAR; PG8_MMA(0, 0, At, B0); PG8_MMA(0, 1, At, B1); PG8_BAR; PG8_SCHED;
.LBB0_1762:
	ds_read_b128 v[24:27], v165
	ds_read_b128 v[28:31], v165 offset:1024
	ds_read_b128 v[16:19], v165 offset:2048
	ds_read_b128 v[20:23], v165 offset:3072
	ds_read_b128 v[8:11], v167
	ds_read_b128 v[12:15], v167 offset:1024
	ds_read_b128 v[0:3], v167 offset:2048
	ds_read_b128 v[4:7], v167 offset:3072
	s_add_i32 s33, s8, 2
	s_cmp_eq_u32 s67, s8
	s_cselect_b32 s36, s28, s75
	s_cselect_b32 s37, s29, s80
	s_cselect_b32 s34, s30, s81
	s_cselect_b32 s35, s31, s82
	s_add_u32 s8, s36, 0x80
	s_addc_u32 s9, s37, 0
	ds_read_b128 v[174:177], v169
	ds_read_b128 v[178:181], v169 offset:1024
	ds_read_b128 v[182:185], v169 offset:2048
	ds_read_b128 v[186:189], v169 offset:3072
	ds_read_b128 v[190:193], v169 offset:4096
	ds_read_b128 v[194:197], v169 offset:5120
	ds_read_b128 v[198:201], v169 offset:6144
	ds_read_b128 v[202:205], v169 offset:7168
	s_mov_b32 m0, s68
	s_nop 0
	global_load_lds_dwordx4 v160, s[6:7]
	s_mov_b32 m0, s69
	s_nop 0
	global_load_lds_dwordx4 v164, s[6:7]
	s_cmp_eq_u32 s101, 0
	s_cbranch_scc1 .Lrxn15_0
	s_waitcnt vmcnt(16)
	s_branch .Lrxj15_0

; #define PG8_STAGE(bufoff, gbase, voff) do { _Pragma("unroll") for (int _i = 0; _i < 2; ++_i) { unsigned keep_; \
;         asm volatile("s_mov_b32 %0, m0\n\ts_mov_b32 m0, %3\n\ts_nop 0\n\tglobal_load_lds_dwordx4 %1, %2\n\ts_mov_b32 m0, %0" : "=&s"(keep_) : "v"((voff)[_i]), "s"((const char*)(gbase)), "s"(ldsb + (unsigned)((bufoff) + _i * 8192)) : "memory"); } } while (0)
; #define PG8_LDA(dst, b, h) do { _Pragma("unroll") for (int m = 0; m < 4; ++m) _Pragma("unroll") for (int k = 0; k < 2; ++k) dst[m][k] = *(const PG8_LAS bf16x8*)(lds + PG8_SA(b, h) + aoff + m * 2048 + k * 1024); } while (0)
; #define PG8_LDB(dst, b, h) do { _Pragma("unroll") for (int n = 0; n < 2; ++n) _Pragma("unroll") for (int k = 0; k < 2; ++k) dst[n][k] = *(const PG8_LAS bf16x8*)(lds + PG8_SB(b, h) + boff + n * 2048 + k * 1024); } while (0)
; #define PG8_WAIT_V(n) asm volatile("s_waitcnt vmcnt(" #n ")" ::: "memory")
; #define PG8_WAIT_L(n) asm volatile("s_waitcnt lgkmcnt(" #n ")" ::: "memory")
; #define PG8_BAR __builtin_amdgcn_s_barrier()
; #define PG8_SCHED __builtin_amdgcn_sched_barrier(0)
; template <class Epi, class Sched, bool ALIGN_EPI, bool FP8 = false>
; __device__ __forceinline__ void gemm_phase(PG8_LAS unsigned char* lds, const Gemm g, const Sched& S, const Epi& E, const int wid, const int lane) {
;     ...
;             PG8_WAIT_V(8); PG8_WAIT_L(0); PG8_BAR; PG8_MMA(1, 0, At, B0); PG8_MMA(1, 1, At, B1); PG8_BAR; PG8_SCHED;
;             PG8_LDB(B0, 1, 0); PG8_LDB(B1, 1, 1); PG8_SCHED; PG8_LDA(At, 1, 0); PG8_STAGE(PG8_SA(0, 1), a2 + hstepA, vc1);
;             PG8_WAIT_V(8); PG8_WAIT_L(0); PG8_BAR; PG8_MMA(0, 0, At, B0); PG8_MMA(0, 1, At, B1); PG8_BAR; PG8_SCHED;
.Lrxj15_1:
	s_mov_b32 s101, 0
	s_waitcnt lgkmcnt(0)
	s_barrier
	s_setprio 1
	s_waitcnt lgkmcnt(6)
	v_mfma_scale_f32_16x16x128_f8f6f4 v[92:95], v[24:31], v[174:181], v[92:95], v170, v171 op_sel_hi:[0,0,0]
	v_mfma_scale_f32_16x16x128_f8f6f4 v[88:91], v[16:23], v[174:181], v[88:91], v170, v171 op_sel_hi:[0,0,0]
	s_waitcnt lgkmcnt(4)
	v_mfma_scale_f32_16x16x128_f8f6f4 v[76:79], v[24:31], v[182:189], v[76:79], v170, v171 op_sel_hi:[0,0,0]
	v_mfma_scale_f32_16x16x128_f8f6f4 v[72:75], v[16:23], v[182:189], v[72:75], v170, v171 op_sel_hi:[0,0,0]
	s_waitcnt lgkmcnt(2)
	v_mfma_scale_f32_16x16x128_f8f6f4 v[60:63], v[24:31], v[190:197], v[60:63], v170, v171 op_sel_hi:[0,0,0]
	v_mfma_scale_f32_16x16x128_f8f6f4 v[56:59], v[16:23], v[190:197], v[56:59], v170, v171 op_sel_hi:[0,0,0]
	s_waitcnt lgkmcnt(0)
	v_mfma_scale_f32_16x16x128_f8f6f4 v[44:47], v[24:31], v[198:205], v[44:47], v170, v171 op_sel_hi:[0,0,0]
	v_mfma_scale_f32_16x16x128_f8f6f4 v[40:43], v[16:23], v[198:205], v[40:43], v170, v171 op_sel_hi:[0,0,0]
	s_setprio 0
	s_setprio 1
	v_mfma_scale_f32_16x16x128_f8f6f4 v[84:87], v[8:15], v[174:181], v[84:87], v170, v171 op_sel_hi:[0,0,0]
	v_mfma_scale_f32_16x16x128_f8f6f4 v[80:83], v[0:7], v[174:181], v[80:83], v170, v171 op_sel_hi:[0,0,0]
	v_mfma_scale_f32_16x16x128_f8f6f4 v[68:71], v[8:15], v[182:189], v[68:71], v170, v171 op_sel_hi:[0,0,0]
	v_mfma_scale_f32_16x16x128_f8f6f4 v[64:67], v[0:7], v[182:189], v[64:67], v170, v171 op_sel_hi:[0,0,0]
	v_mfma_scale_f32_16x16x128_f8f6f4 v[52:55], v[8:15], v[190:197], v[52:55], v170, v171 op_sel_hi:[0,0,0]
	v_mfma_scale_f32_16x16x128_f8f6f4 v[48:51], v[0:7], v[190:197], v[48:51], v170, v171 op_sel_hi:[0,0,0]
	v_mfma_scale_f32_16x16x128_f8f6f4 v[36:39], v[8:15], v[198:205], v[36:39], v170, v171 op_sel_hi:[0,0,0]
	v_mfma_scale_f32_16x16x128_f8f6f4 v[32:35], v[0:7], v[198:205], v[32:35], v170, v171 op_sel_hi:[0,0,0]
	s_setprio 0
	s_barrier
	ds_read_b128 v[0:3], v172
	ds_read_b128 v[4:7], v172 offset:1024
	ds_read_b128 v[8:11], v172 offset:2048
	ds_read_b128 v[12:15], v172 offset:3072
	ds_read_b128 v[16:19], v173
	ds_read_b128 v[20:23], v173 offset:1024
	ds_read_b128 v[24:27], v173 offset:2048
	ds_read_b128 v[28:31], v173 offset:3072
	ds_read_b128 v[174:177], v169 offset:32768
	ds_read_b128 v[178:181], v169 offset:33792
	ds_read_b128 v[182:185], v169 offset:34816
	ds_read_b128 v[186:189], v169 offset:35840
	ds_read_b128 v[190:193], v169 offset:36864
	ds_read_b128 v[194:197], v169 offset:37888
	ds_read_b128 v[198:201], v169 offset:38912
	ds_read_b128 v[202:205], v169 offset:39936
	s_add_u32 s36, s36, s12
	s_addc_u32 s37, s37, s13
	s_mov_b32 m0, s50
	s_nop 0
	global_load_lds_dwordx4 v160, s[36:37]
	s_mov_b32 m0, s51
	s_nop 0
	global_load_lds_dwordx4 v164, s[36:37]
	s_waitcnt vmcnt(8)
	s_waitcnt lgkmcnt(0)
	s_barrier
	s_setprio 1
	s_waitcnt lgkmcnt(6)
	v_mfma_scale_f32_16x16x128_f8f6f4 v[156:159], v[0:7], v[174:181], v[156:159], v170, v171 op_sel_hi:[0,0,0]
	v_mfma_scale_f32_16x16x128_f8f6f4 v[152:155], v[8:15], v[174:181], v[152:155], v170, v171 op_sel_hi:[0,0,0]
	s_waitcnt lgkmcnt(4)
	v_mfma_scale_f32_16x16x128_f8f6f4 v[140:143], v[0:7], v[182:189], v[140:143], v170, v171 op_sel_hi:[0,0,0]
	v_mfma_scale_f32_16x16x128_f8f6f4 v[136:139], v[8:15], v[182:189], v[136:139], v170, v171 op_sel_hi:[0,0,0]
	s_waitcnt lgkmcnt(2)
	v_mfma_scale_f32_16x16x128_f8f6f4 v[124:127], v[0:7], v[190:197], v[124:127], v170, v171 op_sel_hi:[0,0,0]
	v_mfma_scale_f32_16x16x128_f8f6f4 v[120:123], v[8:15], v[190:197], v[120:123], v170, v171 op_sel_hi:[0,0,0]
	s_waitcnt lgkmcnt(0)
	v_mfma_scale_f32_16x16x128_f8f6f4 v[108:111], v[0:7], v[198:205], v[108:111], v170, v171 op_sel_hi:[0,0,0]
	v_mfma_scale_f32_16x16x128_f8f6f4 v[104:107], v[8:15], v[198:205], v[104:107], v170, v171 op_sel_hi:[0,0,0]
	s_setprio 0
	s_setprio 1
	v_mfma_scale_f32_16x16x128_f8f6f4 v[148:151], v[16:23], v[174:181], v[148:151], v170, v171 op_sel_hi:[0,0,0]
	v_mfma_scale_f32_16x16x128_f8f6f4 v[144:147], v[24:31], v[174:181], v[144:147], v170, v171 op_sel_hi:[0,0,0]
	v_mfma_scale_f32_16x16x128_f8f6f4 v[132:135], v[16:23], v[182:189], v[132:135], v170, v171 op_sel_hi:[0,0,0]
	v_mfma_scale_f32_16x16x128_f8f6f4 v[128:131], v[24:31], v[182:189], v[128:131], v170, v171 op_sel_hi:[0,0,0]
	v_mfma_scale_f32_16x16x128_f8f6f4 v[116:119], v[16:23], v[190:197], v[116:119], v170, v171 op_sel_hi:[0,0,0]
	v_mfma_scale_f32_16x16x128_f8f6f4 v[112:115], v[24:31], v[190:197], v[112:115], v170, v171 op_sel_hi:[0,0,0]
	v_mfma_scale_f32_16x16x128_f8f6f4 v[100:103], v[16:23], v[198:205], v[100:103], v170, v171 op_sel_hi:[0,0,0]
	v_mfma_scale_f32_16x16x128_f8f6f4 v[96:99], v[24:31], v[198:205], v[96:99], v170, v171 op_sel_hi:[0,0,0]
	s_setprio 0
	s_barrier
; #define PG8_STAGE(bufoff, gbase, voff) do { _Pragma("unroll") for (int _i = 0; _i < 2; ++_i) { unsigned keep_; \
;         asm volatile("s_mov_b32 %0, m0\n\ts_mov_b32 m0, %3\n\ts_nop 0\n\tglobal_load_lds_dwordx4 %1, %2\n\ts_mov_b32 m0, %0" : "=&s"(keep_) : "v"((voff)[_i]), "s"((const char*)(gbase)), "s"(ldsb + (unsigned)((bufoff) + _i * 8192)) : "memory"); } } while (0)
; #define PG8_LDA(dst, b, h) do { _Pragma("unroll") for (int m = 0; m < 4; ++m) _Pragma("unroll") for (int k = 0; k < 2; ++k) dst[m][k] = *(const PG8_LAS bf16x8*)(lds + PG8_SA(b, h) + aoff + m * 2048 + k * 1024); } while (0)
; #define PG8_WAIT_V(n) asm volatile("s_waitcnt vmcnt(" #n ")" ::: "memory")
; #define PG8_WAIT_L(n) asm volatile("s_waitcnt lgkmcnt(" #n ")" ::: "memory")
; #define PG8_BAR __builtin_amdgcn_s_barrier()
; #define PG8_SCHED __builtin_amdgcn_sched_barrier(0)
; template <class Epi, class Sched, bool ALIGN_EPI, bool FP8 = false>
; __device__ __forceinline__ void gemm_phase(PG8_LAS unsigned char* lds, const Gemm g, const Sched& S, const Epi& E, const int wid, const int lane) {
;     ...
;             PG8_LDA(At, 1, 1); PG8_STAGE(PG8_SB(1, 0), b3, voffB); PG8_STAGE(PG8_SB(1, 1), b3 + hstep, voffB); PG8_STAGE(PG8_SA(1, 0), a3, vc0);
;             PG8_WAIT_V(8); PG8_WAIT_L(0); PG8_BAR; PG8_MMA(1, 0, At, B0); PG8_MMA(1, 1, At, B1); PG8_BAR; PG8_SCHED;
	ds_read_b128 v[174:177], v169 offset:49152
	ds_read_b128 v[178:181], v169 offset:50176
	ds_read_b128 v[182:185], v169 offset:51200
	ds_read_b128 v[186:189], v169 offset:52224
	ds_read_b128 v[190:193], v169 offset:53248
	ds_read_b128 v[194:197], v169 offset:54272
	ds_read_b128 v[198:201], v169 offset:55296
	ds_read_b128 v[202:205], v169 offset:56320
	s_add_u32 s34, s34, 0x80
	s_addc_u32 s35, s35, 0
	s_mov_b32 m0, s53
	s_nop 0
	global_load_lds_dwordx4 v162, s[34:35]
	s_mov_b32 m0, s54
	s_nop 0
	global_load_lds_dwordx4 v166, s[34:35]
	s_add_u32 s34, s34, s12
	s_addc_u32 s35, s35, s13
	s_mov_b32 m0, s65
	s_nop 0
	global_load_lds_dwordx4 v162, s[34:35]
	s_mov_b32 m0, s66
	s_nop 0
	global_load_lds_dwordx4 v166, s[34:35]
	s_mov_b32 m0, s55
	s_nop 0
	global_load_lds_dwordx4 v160, s[8:9]
	s_mov_b32 m0, s64
	s_nop 0
	global_load_lds_dwordx4 v164, s[8:9]
	s_waitcnt vmcnt(8)
	s_waitcnt lgkmcnt(0)
	s_barrier
	s_setprio 1
	s_waitcnt lgkmcnt(6)
	v_mfma_scale_f32_16x16x128_f8f6f4 v[92:95], v[0:7], v[174:181], v[92:95], v170, v171 op_sel_hi:[0,0,0]
	v_mfma_scale_f32_16x16x128_f8f6f4 v[88:91], v[8:15], v[174:181], v[88:91], v170, v171 op_sel_hi:[0,0,0]
	s_waitcnt lgkmcnt(4)
	v_mfma_scale_f32_16x16x128_f8f6f4 v[76:79], v[0:7], v[182:189], v[76:79], v170, v171 op_sel_hi:[0,0,0]
	v_mfma_scale_f32_16x16x128_f8f6f4 v[72:75], v[8:15], v[182:189], v[72:75], v170, v171 op_sel_hi:[0,0,0]
	s_waitcnt lgkmcnt(2)
	v_mfma_scale_f32_16x16x128_f8f6f4 v[60:63], v[0:7], v[190:197], v[60:63], v170, v171 op_sel_hi:[0,0,0]
	v_mfma_scale_f32_16x16x128_f8f6f4 v[56:59], v[8:15], v[190:197], v[56:59], v170, v171 op_sel_hi:[0,0,0]
	s_waitcnt lgkmcnt(0)
	v_mfma_scale_f32_16x16x128_f8f6f4 v[44:47], v[0:7], v[198:205], v[44:47], v170, v171 op_sel_hi:[0,0,0]
	v_mfma_scale_f32_16x16x128_f8f6f4 v[40:43], v[8:15], v[198:205], v[40:43], v170, v171 op_sel_hi:[0,0,0]
	s_setprio 0
	s_setprio 1
	v_mfma_scale_f32_16x16x128_f8f6f4 v[84:87], v[16:23], v[174:181], v[84:87], v170, v171 op_sel_hi:[0,0,0]
	v_mfma_scale_f32_16x16x128_f8f6f4 v[80:83], v[24:31], v[174:181], v[80:83], v170, v171 op_sel_hi:[0,0,0]
	v_mfma_scale_f32_16x16x128_f8f6f4 v[68:71], v[16:23], v[182:189], v[68:71], v170, v171 op_sel_hi:[0,0,0]
	v_mfma_scale_f32_16x16x128_f8f6f4 v[64:67], v[24:31], v[182:189], v[64:67], v170, v171 op_sel_hi:[0,0,0]
	v_mfma_scale_f32_16x16x128_f8f6f4 v[52:55], v[16:23], v[190:197], v[52:55], v170, v171 op_sel_hi:[0,0,0]
	v_mfma_scale_f32_16x16x128_f8f6f4 v[48:51], v[24:31], v[190:197], v[48:51], v170, v171 op_sel_hi:[0,0,0]
	v_mfma_scale_f32_16x16x128_f8f6f4 v[36:39], v[16:23], v[198:205], v[36:39], v170, v171 op_sel_hi:[0,0,0]
	v_mfma_scale_f32_16x16x128_f8f6f4 v[32:35], v[24:31], v[198:205], v[32:35], v170, v171 op_sel_hi:[0,0,0]
	s_setprio 0
	s_barrier
	s_add_u32 s75, s75, 0x100
	s_addc_u32 s80, s80, 0
	s_add_u32 s81, s81, 0x100
	s_addc_u32 s82, s82, 0
	s_add_u32 s6, s6, 0x100
	s_addc_u32 s7, s7, 0
	s_cmp_ge_i32 s33, s52
	s_mov_b32 s8, s33
	s_cbranch_scc0 .LBB0_1762
